# v28 + attention epilogue lane-pair exchange by DPP instead of LDS bpermute
# baseline (speedup 1.0000x reference)
; __device__ __forceinline__ int crow(int r, int hi) { return (r & 3) + 8 * (r >> 2) + 4 * hi; }
; __device__ __forceinline__ unsigned cvtpk(float lo, float hi) { unsigned r; asm volatile("v_cvt_pk_bf16_f32 %0, %1, %2" : "=v"(r) : "v"(lo), "v"(hi)); return r; }
; template <int MODE>
; __device__ __forceinline__ void attn_block_pipe(const BlockRef& cur, const BlockRef& nxt, char* lds, LAS unsigned char* ldsl, Seam<MODE>& S) {
;     ...
;     if (hi == 0) li_l[r32] = l_reg; asm volatile("s_waitcnt lgkmcnt(0)" ::: "memory");
;     if constexpr (C::ALIBI) { if (hi == 0) cur.LSE[(size_t)(qlo + r32) * cur.ls] = m_reg * SCALE + __logf(l_reg); }
;     float rli[16];
; #pragma unroll
;     for (int r = 0; r < 16; ++r) rli[r] = __builtin_amdgcn_rcpf(li_l[crow(r, hi)]);
;     bf16_t* Ow = cur.O + (size_t)qlo * cur.os;
;     const unsigned ol_ = (unsigned)(4 * hi * cur.os + r32) * 2u;
; #pragma unroll
;     for (int r = 0; r < 16; ++r) { const size_t ou_ = (size_t)((r & 3) + 8 * (r >> 2)) * cur.os;
; #pragma unroll
;         for (int d0 = 0; d0 < 4; ++d0) { const float v = o[d0][r] * rli[r];
;             const float vn = __shfl_xor(v, 1);
;             if ((r32 & 1) == 0) *(unsigned*)((char*)(Ow + ou_ + d0 * 32) + ol_) = cvtpk(v, vn); } }
.LBB0_551:
	s_waitcnt vmcnt(12)
	v_cmp_gt_u32_e32 vcc, 32, v207
	s_and_saveexec_b64 s[4:5], vcc
	ds_write_b32 v209, v2
	s_or_b64 exec, exec, s[4:5]
	s_waitcnt lgkmcnt(0)
	ds_read_b128 v[94:97], v208
	v_and_b32_e32 v17, 64, v1
	v_xor_b32_e32 v16, 1, v1
	v_add_u32_e32 v17, 64, v17
	v_cmp_lt_i32_e32 vcc, v16, v17
	s_waitcnt lgkmcnt(0)
	v_rcp_f32_e32 v98, v94
	ds_read_b128 v[90:93], v208 offset:32
	ds_read_b128 v[86:89], v208 offset:64
	ds_read_b128 v[82:85], v208 offset:96
	v_cndmask_b32_e32 v16, v1, v16, vcc
	v_lshlrev_b32_e32 v94, 2, v16
	v_mul_f32_e32 v66, v66, v98
	s_ashr_i32 s47, s46, 31
	s_nop 1
	v_mov_b32_dpp v99, v66 quad_perm:[1,0,3,2] row_mask:0xf bank_mask:0xf bound_ctrl:1
	s_lshl_b64 s[4:5], s[46:47], 11
	s_add_u32 s6, s44, s4
	v_lshlrev_b32_e32 v2, 1, v205
	s_addc_u32 s7, s45, s5
	v_lshl_or_b32 v2, v204, 13, v2
	v_and_b32_e32 v16, 1, v203
	v_cmp_eq_u32_e64 s[4:5], 0, v16
	v_lshl_add_u64 v[16:17], s[6:7], 0, v[2:3]
	s_and_saveexec_b64 s[6:7], s[4:5]
	s_cbranch_execz .LBB0_555
	s_waitcnt lgkmcnt(0)
	v_cvt_pk_bf16_f32 v2, v66, v99
	global_store_dword v[16:17], v2, off
.LBB0_555:
	s_or_b64 exec, exec, s[6:7]
	v_mul_f32_e32 v2, v50, v98
	s_nop 1
	v_mov_b32_dpp v50, v2 quad_perm:[1,0,3,2] row_mask:0xf bank_mask:0xf bound_ctrl:1
	s_and_saveexec_b64 s[6:7], s[4:5]
	s_cbranch_execz .LBB0_557
	s_waitcnt lgkmcnt(0)
	v_cvt_pk_bf16_f32 v2, v2, v50
	global_store_dword v[16:17], v2, off offset:64
.LBB0_557:
	s_or_b64 exec, exec, s[6:7]
	v_mul_f32_e32 v2, v34, v98
	s_nop 1
	v_mov_b32_dpp v34, v2 quad_perm:[1,0,3,2] row_mask:0xf bank_mask:0xf bound_ctrl:1
	s_and_saveexec_b64 s[6:7], s[4:5]
	s_cbranch_execz .LBB0_559
	s_waitcnt lgkmcnt(0)
	v_cvt_pk_bf16_f32 v2, v2, v34
	global_store_dword v[16:17], v2, off offset:128
.LBB0_559:
	s_or_b64 exec, exec, s[6:7]
	v_mul_f32_e32 v2, v18, v98
	s_nop 1
	v_mov_b32_dpp v18, v2 quad_perm:[1,0,3,2] row_mask:0xf bank_mask:0xf bound_ctrl:1
	s_and_saveexec_b64 s[6:7], s[4:5]
	s_cbranch_execz .LBB0_561
	s_waitcnt lgkmcnt(0)
	v_cvt_pk_bf16_f32 v2, v2, v18
	global_store_dword v[16:17], v2, off offset:192
.LBB0_561:
	s_or_b64 exec, exec, s[6:7]
	v_rcp_f32_e32 v2, v95
	s_waitcnt lgkmcnt(0)
	v_mul_f32_e32 v18, v67, v2
	s_nop 1
	v_mov_b32_dpp v34, v18 quad_perm:[1,0,3,2] row_mask:0xf bank_mask:0xf bound_ctrl:1
	s_and_saveexec_b64 s[6:7], s[4:5]
	s_cbranch_execz .LBB0_563
	s_waitcnt lgkmcnt(0)
	v_cvt_pk_bf16_f32 v18, v18, v34
	global_store_dword v[16:17], v18, off offset:2048
.LBB0_563:
	s_or_b64 exec, exec, s[6:7]
	v_mul_f32_e32 v18, v51, v2
	s_waitcnt lgkmcnt(0)
	s_nop 1
	v_mov_b32_dpp v34, v18 quad_perm:[1,0,3,2] row_mask:0xf bank_mask:0xf bound_ctrl:1
	s_and_saveexec_b64 s[6:7], s[4:5]
	s_cbranch_execz .LBB0_565
	s_waitcnt lgkmcnt(0)
	v_cvt_pk_bf16_f32 v18, v18, v34
	global_store_dword v[16:17], v18, off offset:2112
.LBB0_565:
	s_or_b64 exec, exec, s[6:7]
	v_mul_f32_e32 v18, v35, v2
	s_waitcnt lgkmcnt(0)
	s_nop 1
	v_mov_b32_dpp v34, v18 quad_perm:[1,0,3,2] row_mask:0xf bank_mask:0xf bound_ctrl:1
	s_and_saveexec_b64 s[6:7], s[4:5]
	s_cbranch_execz .LBB0_567
	s_waitcnt lgkmcnt(0)
	v_cvt_pk_bf16_f32 v18, v18, v34
	global_store_dword v[16:17], v18, off offset:2176
.LBB0_567:
	s_or_b64 exec, exec, s[6:7]
	v_mul_f32_e32 v2, v19, v2
	s_nop 1
	v_mov_b32_dpp v18, v2 quad_perm:[1,0,3,2] row_mask:0xf bank_mask:0xf bound_ctrl:1
	s_and_saveexec_b64 s[6:7], s[4:5]
	s_cbranch_execz .LBB0_569
	s_waitcnt lgkmcnt(0)
	v_cvt_pk_bf16_f32 v2, v2, v18
	global_store_dword v[16:17], v2, off offset:2240
.LBB0_569:
	s_or_b64 exec, exec, s[6:7]
	v_rcp_f32_e32 v2, v96
	s_waitcnt lgkmcnt(0)
	v_mul_f32_e32 v18, v68, v2
	s_nop 1
	v_mov_b32_dpp v19, v18 quad_perm:[1,0,3,2] row_mask:0xf bank_mask:0xf bound_ctrl:1
	s_and_saveexec_b64 s[6:7], s[4:5]
	s_cbranch_execz .LBB0_571
	s_waitcnt lgkmcnt(0)
	v_cvt_pk_bf16_f32 v34, v18, v19
	v_add_co_u32_e32 v18, vcc, 0x1000, v16
	s_nop 1
	v_addc_co_u32_e32 v19, vcc, 0, v17, vcc
	global_store_dword v[18:19], v34, off
.LBB0_571:
	s_or_b64 exec, exec, s[6:7]
	v_mul_f32_e32 v18, v52, v2
	s_waitcnt lgkmcnt(0)
	s_nop 1
	v_mov_b32_dpp v19, v18 quad_perm:[1,0,3,2] row_mask:0xf bank_mask:0xf bound_ctrl:1
	s_and_saveexec_b64 s[6:7], s[4:5]
	s_cbranch_execz .LBB0_573
	s_waitcnt lgkmcnt(0)
	v_cvt_pk_bf16_f32 v34, v18, v19
	v_add_co_u32_e32 v18, vcc, 0x1000, v16
	s_nop 1
	v_addc_co_u32_e32 v19, vcc, 0, v17, vcc
	global_store_dword v[18:19], v34, off offset:64
.LBB0_573:
	s_or_b64 exec, exec, s[6:7]
	v_mul_f32_e32 v18, v36, v2
	s_waitcnt lgkmcnt(0)
	s_nop 1
	v_mov_b32_dpp v19, v18 quad_perm:[1,0,3,2] row_mask:0xf bank_mask:0xf bound_ctrl:1
	s_and_saveexec_b64 s[6:7], s[4:5]
	s_cbranch_execz .LBB0_575
	s_waitcnt lgkmcnt(0)
	v_cvt_pk_bf16_f32 v34, v18, v19
	v_add_co_u32_e32 v18, vcc, 0x1000, v16
	s_nop 1
	v_addc_co_u32_e32 v19, vcc, 0, v17, vcc
	global_store_dword v[18:19], v34, off offset:128
.LBB0_575:
	s_or_b64 exec, exec, s[6:7]
	v_mul_f32_e32 v2, v20, v2
	s_nop 1
	v_mov_b32_dpp v18, v2 quad_perm:[1,0,3,2] row_mask:0xf bank_mask:0xf bound_ctrl:1
	s_and_saveexec_b64 s[6:7], s[4:5]
	s_cbranch_execz .LBB0_577
	s_waitcnt lgkmcnt(0)
	v_cvt_pk_bf16_f32 v2, v2, v18
	v_add_co_u32_e32 v18, vcc, 0x1000, v16
	s_nop 1
	v_addc_co_u32_e32 v19, vcc, 0, v17, vcc
	global_store_dword v[18:19], v2, off offset:192
.LBB0_577:
	s_or_b64 exec, exec, s[6:7]
	v_rcp_f32_e32 v2, v97
	s_waitcnt lgkmcnt(0)
	v_mul_f32_e32 v18, v69, v2
	s_nop 1
	v_mov_b32_dpp v19, v18 quad_perm:[1,0,3,2] row_mask:0xf bank_mask:0xf bound_ctrl:1
	s_and_saveexec_b64 s[6:7], s[4:5]
	s_cbranch_execz .LBB0_579
	s_waitcnt lgkmcnt(0)
	v_cvt_pk_bf16_f32 v20, v18, v19
	v_add_co_u32_e32 v18, vcc, 0x1000, v16
	s_nop 1
	v_addc_co_u32_e32 v19, vcc, 0, v17, vcc
	global_store_dword v[18:19], v20, off offset:2048
; __device__ __forceinline__ unsigned cvtpk(float lo, float hi) { unsigned r; asm volatile("v_cvt_pk_bf16_f32 %0, %1, %2" : "=v"(r) : "v"(lo), "v"(hi)); return r; }
; template <int MODE>
; __device__ __forceinline__ void attn_block_pipe(const BlockRef& cur, const BlockRef& nxt, char* lds, LAS unsigned char* ldsl, Seam<MODE>& S) {
;     ...
; #pragma unroll
;     for (int r = 0; r < 16; ++r) { const size_t ou_ = (size_t)((r & 3) + 8 * (r >> 2)) * cur.os;
; #pragma unroll
;         for (int d0 = 0; d0 < 4; ++d0) { const float v = o[d0][r] * rli[r];
;             const float vn = __shfl_xor(v, 1);
;             if ((r32 & 1) == 0) *(unsigned*)((char*)(Ow + ou_ + d0 * 32) + ol_) = cvtpk(v, vn); } }
.LBB0_579:
	s_or_b64 exec, exec, s[6:7]
	v_mul_f32_e32 v18, v53, v2
	s_waitcnt lgkmcnt(0)
	s_nop 1
	v_mov_b32_dpp v19, v18 quad_perm:[1,0,3,2] row_mask:0xf bank_mask:0xf bound_ctrl:1
	s_and_saveexec_b64 s[6:7], s[4:5]
	s_cbranch_execz .LBB0_581
	s_waitcnt lgkmcnt(0)
	v_cvt_pk_bf16_f32 v20, v18, v19
	v_add_co_u32_e32 v18, vcc, 0x1000, v16
	s_nop 1
	v_addc_co_u32_e32 v19, vcc, 0, v17, vcc
	global_store_dword v[18:19], v20, off offset:2112
.LBB0_581:
	s_or_b64 exec, exec, s[6:7]
	v_mul_f32_e32 v18, v37, v2
	s_waitcnt lgkmcnt(0)
	s_nop 1
	v_mov_b32_dpp v19, v18 quad_perm:[1,0,3,2] row_mask:0xf bank_mask:0xf bound_ctrl:1
	s_and_saveexec_b64 s[6:7], s[4:5]
	s_cbranch_execz .LBB0_583
	s_waitcnt lgkmcnt(0)
	v_cvt_pk_bf16_f32 v20, v18, v19
	v_add_co_u32_e32 v18, vcc, 0x1000, v16
	s_nop 1
	v_addc_co_u32_e32 v19, vcc, 0, v17, vcc
	global_store_dword v[18:19], v20, off offset:2176
.LBB0_583:
	s_or_b64 exec, exec, s[6:7]
	v_mul_f32_e32 v2, v21, v2
	s_nop 1
	v_mov_b32_dpp v18, v2 quad_perm:[1,0,3,2] row_mask:0xf bank_mask:0xf bound_ctrl:1
	s_and_saveexec_b64 s[6:7], s[4:5]
	s_cbranch_execz .LBB0_585
	s_waitcnt lgkmcnt(0)
	v_cvt_pk_bf16_f32 v2, v2, v18
	v_add_co_u32_e32 v18, vcc, 0x1000, v16
	s_nop 1
	v_addc_co_u32_e32 v19, vcc, 0, v17, vcc
	global_store_dword v[18:19], v2, off offset:2240
.LBB0_585:
	s_or_b64 exec, exec, s[6:7]
	v_rcp_f32_e32 v2, v90
	s_waitcnt lgkmcnt(0)
	v_mul_f32_e32 v18, v70, v2
	s_nop 1
	v_mov_b32_dpp v19, v18 quad_perm:[1,0,3,2] row_mask:0xf bank_mask:0xf bound_ctrl:1
	s_and_saveexec_b64 s[6:7], s[4:5]
	s_cbranch_execz .LBB0_587
	s_waitcnt lgkmcnt(0)
	v_cvt_pk_bf16_f32 v20, v18, v19
	v_add_co_u32_e32 v18, vcc, 0x4000, v16
	s_nop 1
	v_addc_co_u32_e32 v19, vcc, 0, v17, vcc
	global_store_dword v[18:19], v20, off
.LBB0_587:
	s_or_b64 exec, exec, s[6:7]
	v_mul_f32_e32 v18, v54, v2
	s_waitcnt lgkmcnt(0)
	s_nop 1
	v_mov_b32_dpp v19, v18 quad_perm:[1,0,3,2] row_mask:0xf bank_mask:0xf bound_ctrl:1
	s_and_saveexec_b64 s[6:7], s[4:5]
	s_cbranch_execz .LBB0_589
	s_waitcnt lgkmcnt(0)
	v_cvt_pk_bf16_f32 v20, v18, v19
	v_add_co_u32_e32 v18, vcc, 0x4000, v16
	s_nop 1
	v_addc_co_u32_e32 v19, vcc, 0, v17, vcc
	global_store_dword v[18:19], v20, off offset:64
.LBB0_589:
	s_or_b64 exec, exec, s[6:7]
	v_mul_f32_e32 v18, v38, v2
	s_waitcnt lgkmcnt(0)
	s_nop 1
	v_mov_b32_dpp v19, v18 quad_perm:[1,0,3,2] row_mask:0xf bank_mask:0xf bound_ctrl:1
	s_and_saveexec_b64 s[6:7], s[4:5]
	s_cbranch_execz .LBB0_591
	s_waitcnt lgkmcnt(0)
	v_cvt_pk_bf16_f32 v20, v18, v19
	v_add_co_u32_e32 v18, vcc, 0x4000, v16
	s_nop 1
	v_addc_co_u32_e32 v19, vcc, 0, v17, vcc
	global_store_dword v[18:19], v20, off offset:128
.LBB0_591:
	s_or_b64 exec, exec, s[6:7]
	v_mul_f32_e32 v2, v22, v2
	s_nop 1
	v_mov_b32_dpp v18, v2 quad_perm:[1,0,3,2] row_mask:0xf bank_mask:0xf bound_ctrl:1
	s_and_saveexec_b64 s[6:7], s[4:5]
	s_cbranch_execz .LBB0_593
	s_waitcnt lgkmcnt(0)
	v_cvt_pk_bf16_f32 v2, v2, v18
	v_add_co_u32_e32 v18, vcc, 0x4000, v16
	s_nop 1
	v_addc_co_u32_e32 v19, vcc, 0, v17, vcc
	global_store_dword v[18:19], v2, off offset:192
.LBB0_593:
	s_or_b64 exec, exec, s[6:7]
	v_rcp_f32_e32 v2, v91
	s_waitcnt lgkmcnt(0)
	v_mul_f32_e32 v18, v71, v2
	s_nop 1
	v_mov_b32_dpp v19, v18 quad_perm:[1,0,3,2] row_mask:0xf bank_mask:0xf bound_ctrl:1
	s_and_saveexec_b64 s[6:7], s[4:5]
	s_cbranch_execz .LBB0_595
	s_waitcnt lgkmcnt(0)
	v_cvt_pk_bf16_f32 v20, v18, v19
	v_add_co_u32_e32 v18, vcc, 0x4000, v16
	s_nop 1
	v_addc_co_u32_e32 v19, vcc, 0, v17, vcc
	global_store_dword v[18:19], v20, off offset:2048
.LBB0_595:
	s_or_b64 exec, exec, s[6:7]
	v_mul_f32_e32 v18, v55, v2
	s_waitcnt lgkmcnt(0)
	s_nop 1
	v_mov_b32_dpp v19, v18 quad_perm:[1,0,3,2] row_mask:0xf bank_mask:0xf bound_ctrl:1
	s_and_saveexec_b64 s[6:7], s[4:5]
	s_cbranch_execz .LBB0_597
	s_waitcnt lgkmcnt(0)
	v_cvt_pk_bf16_f32 v20, v18, v19
	v_add_co_u32_e32 v18, vcc, 0x4000, v16
	s_nop 1
	v_addc_co_u32_e32 v19, vcc, 0, v17, vcc
	global_store_dword v[18:19], v20, off offset:2112
.LBB0_597:
	s_or_b64 exec, exec, s[6:7]
	v_mul_f32_e32 v18, v39, v2
	s_waitcnt lgkmcnt(0)
	s_nop 1
	v_mov_b32_dpp v19, v18 quad_perm:[1,0,3,2] row_mask:0xf bank_mask:0xf bound_ctrl:1
	s_and_saveexec_b64 s[6:7], s[4:5]
	s_cbranch_execz .LBB0_599
	s_waitcnt lgkmcnt(0)
	v_cvt_pk_bf16_f32 v20, v18, v19
	v_add_co_u32_e32 v18, vcc, 0x4000, v16
	s_nop 1
	v_addc_co_u32_e32 v19, vcc, 0, v17, vcc
	global_store_dword v[18:19], v20, off offset:2176
.LBB0_599:
	s_or_b64 exec, exec, s[6:7]
	v_mul_f32_e32 v2, v23, v2
	s_nop 1
	v_mov_b32_dpp v18, v2 quad_perm:[1,0,3,2] row_mask:0xf bank_mask:0xf bound_ctrl:1
	s_and_saveexec_b64 s[6:7], s[4:5]
	s_cbranch_execz .LBB0_601
	s_waitcnt lgkmcnt(0)
	v_cvt_pk_bf16_f32 v2, v2, v18
	v_add_co_u32_e32 v18, vcc, 0x4000, v16
	s_nop 1
	v_addc_co_u32_e32 v19, vcc, 0, v17, vcc
	global_store_dword v[18:19], v2, off offset:2240
.LBB0_601:
	s_or_b64 exec, exec, s[6:7]
	v_rcp_f32_e32 v2, v92
	s_waitcnt lgkmcnt(0)
	v_mul_f32_e32 v18, v72, v2
	s_nop 1
	v_mov_b32_dpp v19, v18 quad_perm:[1,0,3,2] row_mask:0xf bank_mask:0xf bound_ctrl:1
	s_and_saveexec_b64 s[6:7], s[4:5]
	s_cbranch_execz .LBB0_603
	s_waitcnt lgkmcnt(0)
	v_cvt_pk_bf16_f32 v20, v18, v19
	v_add_co_u32_e32 v18, vcc, 0x5000, v16
	s_nop 1
	v_addc_co_u32_e32 v19, vcc, 0, v17, vcc
	global_store_dword v[18:19], v20, off
.LBB0_603:
	s_or_b64 exec, exec, s[6:7]
	v_mul_f32_e32 v18, v56, v2
	s_waitcnt lgkmcnt(0)
	s_nop 1
	v_mov_b32_dpp v19, v18 quad_perm:[1,0,3,2] row_mask:0xf bank_mask:0xf bound_ctrl:1
	s_and_saveexec_b64 s[6:7], s[4:5]
	s_cbranch_execz .LBB0_605
	s_waitcnt lgkmcnt(0)
	v_cvt_pk_bf16_f32 v20, v18, v19
	v_add_co_u32_e32 v18, vcc, 0x5000, v16
	s_nop 1
	v_addc_co_u32_e32 v19, vcc, 0, v17, vcc
	global_store_dword v[18:19], v20, off offset:64
; __device__ __forceinline__ unsigned cvtpk(float lo, float hi) { unsigned r; asm volatile("v_cvt_pk_bf16_f32 %0, %1, %2" : "=v"(r) : "v"(lo), "v"(hi)); return r; }
; template <int MODE>
; __device__ __forceinline__ void attn_block_pipe(const BlockRef& cur, const BlockRef& nxt, char* lds, LAS unsigned char* ldsl, Seam<MODE>& S) {
;     ...
; #pragma unroll
;     for (int r = 0; r < 16; ++r) { const size_t ou_ = (size_t)((r & 3) + 8 * (r >> 2)) * cur.os;
; #pragma unroll
;         for (int d0 = 0; d0 < 4; ++d0) { const float v = o[d0][r] * rli[r];
;             const float vn = __shfl_xor(v, 1);
;             if ((r32 & 1) == 0) *(unsigned*)((char*)(Ow + ou_ + d0 * 32) + ol_) = cvtpk(v, vn); } }
.LBB0_605:
	s_or_b64 exec, exec, s[6:7]
	v_mul_f32_e32 v18, v40, v2
	s_waitcnt lgkmcnt(0)
	s_nop 1
	v_mov_b32_dpp v19, v18 quad_perm:[1,0,3,2] row_mask:0xf bank_mask:0xf bound_ctrl:1
	s_and_saveexec_b64 s[6:7], s[4:5]
	s_cbranch_execz .LBB0_607
	s_waitcnt lgkmcnt(0)
	v_cvt_pk_bf16_f32 v20, v18, v19
	v_add_co_u32_e32 v18, vcc, 0x5000, v16
	s_nop 1
	v_addc_co_u32_e32 v19, vcc, 0, v17, vcc
	global_store_dword v[18:19], v20, off offset:128
.LBB0_607:
	s_or_b64 exec, exec, s[6:7]
	v_mul_f32_e32 v2, v24, v2
	s_nop 1
	v_mov_b32_dpp v18, v2 quad_perm:[1,0,3,2] row_mask:0xf bank_mask:0xf bound_ctrl:1
	s_and_saveexec_b64 s[6:7], s[4:5]
	s_cbranch_execz .LBB0_609
	s_waitcnt lgkmcnt(0)
	v_cvt_pk_bf16_f32 v2, v2, v18
	v_add_co_u32_e32 v18, vcc, 0x5000, v16
	s_nop 1
	v_addc_co_u32_e32 v19, vcc, 0, v17, vcc
	global_store_dword v[18:19], v2, off offset:192
.LBB0_609:
	s_or_b64 exec, exec, s[6:7]
	v_rcp_f32_e32 v2, v93
	s_waitcnt lgkmcnt(0)
	v_mul_f32_e32 v18, v73, v2
	s_nop 1
	v_mov_b32_dpp v19, v18 quad_perm:[1,0,3,2] row_mask:0xf bank_mask:0xf bound_ctrl:1
	s_and_saveexec_b64 s[6:7], s[4:5]
	s_cbranch_execz .LBB0_611
	s_waitcnt lgkmcnt(0)
	v_cvt_pk_bf16_f32 v20, v18, v19
	v_add_co_u32_e32 v18, vcc, 0x5000, v16
	s_nop 1
	v_addc_co_u32_e32 v19, vcc, 0, v17, vcc
	global_store_dword v[18:19], v20, off offset:2048
.LBB0_611:
	s_or_b64 exec, exec, s[6:7]
	v_mul_f32_e32 v18, v57, v2
	s_waitcnt lgkmcnt(0)
	s_nop 1
	v_mov_b32_dpp v19, v18 quad_perm:[1,0,3,2] row_mask:0xf bank_mask:0xf bound_ctrl:1
	s_and_saveexec_b64 s[6:7], s[4:5]
	s_cbranch_execz .LBB0_613
	s_waitcnt lgkmcnt(0)
	v_cvt_pk_bf16_f32 v20, v18, v19
	v_add_co_u32_e32 v18, vcc, 0x5000, v16
	s_nop 1
	v_addc_co_u32_e32 v19, vcc, 0, v17, vcc
	global_store_dword v[18:19], v20, off offset:2112
.LBB0_613:
	s_or_b64 exec, exec, s[6:7]
	v_mul_f32_e32 v18, v41, v2
	s_waitcnt lgkmcnt(0)
	s_nop 1
	v_mov_b32_dpp v19, v18 quad_perm:[1,0,3,2] row_mask:0xf bank_mask:0xf bound_ctrl:1
	s_and_saveexec_b64 s[6:7], s[4:5]
	s_cbranch_execz .LBB0_615
	s_waitcnt lgkmcnt(0)
	v_cvt_pk_bf16_f32 v20, v18, v19
	v_add_co_u32_e32 v18, vcc, 0x5000, v16
	s_nop 1
	v_addc_co_u32_e32 v19, vcc, 0, v17, vcc
	global_store_dword v[18:19], v20, off offset:2176
.LBB0_615:
	s_or_b64 exec, exec, s[6:7]
	v_mul_f32_e32 v2, v25, v2
	s_nop 1
	v_mov_b32_dpp v18, v2 quad_perm:[1,0,3,2] row_mask:0xf bank_mask:0xf bound_ctrl:1
	s_and_saveexec_b64 s[6:7], s[4:5]
	s_cbranch_execz .LBB0_617
	s_waitcnt lgkmcnt(0)
	v_cvt_pk_bf16_f32 v2, v2, v18
	v_add_co_u32_e32 v18, vcc, 0x5000, v16
	s_nop 1
	v_addc_co_u32_e32 v19, vcc, 0, v17, vcc
	global_store_dword v[18:19], v2, off offset:2240
.LBB0_617:
	s_or_b64 exec, exec, s[6:7]
	v_rcp_f32_e32 v2, v86
	s_waitcnt lgkmcnt(0)
	v_mul_f32_e32 v18, v74, v2
	s_nop 1
	v_mov_b32_dpp v19, v18 quad_perm:[1,0,3,2] row_mask:0xf bank_mask:0xf bound_ctrl:1
	s_and_saveexec_b64 s[6:7], s[4:5]
	s_cbranch_execz .LBB0_619
	s_waitcnt lgkmcnt(0)
	v_cvt_pk_bf16_f32 v20, v18, v19
	v_add_co_u32_e32 v18, vcc, 0x8000, v16
	s_nop 1
	v_addc_co_u32_e32 v19, vcc, 0, v17, vcc
	global_store_dword v[18:19], v20, off
.LBB0_619:
	s_or_b64 exec, exec, s[6:7]
	v_mul_f32_e32 v18, v58, v2
	s_waitcnt lgkmcnt(0)
	s_nop 1
	v_mov_b32_dpp v19, v18 quad_perm:[1,0,3,2] row_mask:0xf bank_mask:0xf bound_ctrl:1
	s_and_saveexec_b64 s[6:7], s[4:5]
	s_cbranch_execz .LBB0_621
	s_waitcnt lgkmcnt(0)
	v_cvt_pk_bf16_f32 v20, v18, v19
	v_add_co_u32_e32 v18, vcc, 0x8000, v16
	s_nop 1
	v_addc_co_u32_e32 v19, vcc, 0, v17, vcc
	global_store_dword v[18:19], v20, off offset:64
.LBB0_621:
	s_or_b64 exec, exec, s[6:7]
	v_mul_f32_e32 v18, v42, v2
	s_waitcnt lgkmcnt(0)
	s_nop 1
	v_mov_b32_dpp v19, v18 quad_perm:[1,0,3,2] row_mask:0xf bank_mask:0xf bound_ctrl:1
	s_and_saveexec_b64 s[6:7], s[4:5]
	s_cbranch_execz .LBB0_623
	s_waitcnt lgkmcnt(0)
	v_cvt_pk_bf16_f32 v20, v18, v19
	v_add_co_u32_e32 v18, vcc, 0x8000, v16
	s_nop 1
	v_addc_co_u32_e32 v19, vcc, 0, v17, vcc
	global_store_dword v[18:19], v20, off offset:128
.LBB0_623:
	s_or_b64 exec, exec, s[6:7]
	v_mul_f32_e32 v2, v26, v2
	s_nop 1
	v_mov_b32_dpp v18, v2 quad_perm:[1,0,3,2] row_mask:0xf bank_mask:0xf bound_ctrl:1
	s_and_saveexec_b64 s[6:7], s[4:5]
	s_cbranch_execz .LBB0_625
	s_waitcnt lgkmcnt(0)
	v_cvt_pk_bf16_f32 v2, v2, v18
	v_add_co_u32_e32 v18, vcc, 0x8000, v16
	s_nop 1
	v_addc_co_u32_e32 v19, vcc, 0, v17, vcc
	global_store_dword v[18:19], v2, off offset:192
.LBB0_625:
	s_or_b64 exec, exec, s[6:7]
	v_rcp_f32_e32 v2, v87
	s_waitcnt lgkmcnt(0)
	v_mul_f32_e32 v18, v75, v2
	s_nop 1
	v_mov_b32_dpp v19, v18 quad_perm:[1,0,3,2] row_mask:0xf bank_mask:0xf bound_ctrl:1
	s_and_saveexec_b64 s[6:7], s[4:5]
	s_cbranch_execz .LBB0_627
	s_waitcnt lgkmcnt(0)
	v_cvt_pk_bf16_f32 v20, v18, v19
	v_add_co_u32_e32 v18, vcc, 0x8000, v16
	s_nop 1
	v_addc_co_u32_e32 v19, vcc, 0, v17, vcc
	global_store_dword v[18:19], v20, off offset:2048
.LBB0_627:
	s_or_b64 exec, exec, s[6:7]
	v_mul_f32_e32 v18, v59, v2
	s_waitcnt lgkmcnt(0)
	s_nop 1
	v_mov_b32_dpp v19, v18 quad_perm:[1,0,3,2] row_mask:0xf bank_mask:0xf bound_ctrl:1
	s_and_saveexec_b64 s[6:7], s[4:5]
	s_cbranch_execz .LBB0_629
	s_waitcnt lgkmcnt(0)
	v_cvt_pk_bf16_f32 v20, v18, v19
	v_add_co_u32_e32 v18, vcc, 0x8000, v16
	s_nop 1
	v_addc_co_u32_e32 v19, vcc, 0, v17, vcc
	global_store_dword v[18:19], v20, off offset:2112
.LBB0_629:
	s_or_b64 exec, exec, s[6:7]
	v_mul_f32_e32 v18, v43, v2
	s_waitcnt lgkmcnt(0)
	s_nop 1
	v_mov_b32_dpp v19, v18 quad_perm:[1,0,3,2] row_mask:0xf bank_mask:0xf bound_ctrl:1
	s_and_saveexec_b64 s[6:7], s[4:5]
	s_cbranch_execz .LBB0_631
	s_waitcnt lgkmcnt(0)
	v_cvt_pk_bf16_f32 v20, v18, v19
	v_add_co_u32_e32 v18, vcc, 0x8000, v16
	s_nop 1
	v_addc_co_u32_e32 v19, vcc, 0, v17, vcc
	global_store_dword v[18:19], v20, off offset:2176
; __device__ __forceinline__ unsigned cvtpk(float lo, float hi) { unsigned r; asm volatile("v_cvt_pk_bf16_f32 %0, %1, %2" : "=v"(r) : "v"(lo), "v"(hi)); return r; }
; template <int MODE>
; __device__ __forceinline__ void attn_block_pipe(const BlockRef& cur, const BlockRef& nxt, char* lds, LAS unsigned char* ldsl, Seam<MODE>& S) {
;     ...
; #pragma unroll
;     for (int r = 0; r < 16; ++r) { const size_t ou_ = (size_t)((r & 3) + 8 * (r >> 2)) * cur.os;
; #pragma unroll
;         for (int d0 = 0; d0 < 4; ++d0) { const float v = o[d0][r] * rli[r];
;             const float vn = __shfl_xor(v, 1);
;             if ((r32 & 1) == 0) *(unsigned*)((char*)(Ow + ou_ + d0 * 32) + ol_) = cvtpk(v, vn); } }
.LBB0_631:
	s_or_b64 exec, exec, s[6:7]
	v_mul_f32_e32 v2, v27, v2
	s_nop 1
	v_mov_b32_dpp v18, v2 quad_perm:[1,0,3,2] row_mask:0xf bank_mask:0xf bound_ctrl:1
	s_and_saveexec_b64 s[6:7], s[4:5]
	s_cbranch_execz .LBB0_633
	s_waitcnt lgkmcnt(0)
	v_cvt_pk_bf16_f32 v2, v2, v18
	v_add_co_u32_e32 v18, vcc, 0x8000, v16
	s_nop 1
	v_addc_co_u32_e32 v19, vcc, 0, v17, vcc
	global_store_dword v[18:19], v2, off offset:2240
.LBB0_633:
	s_or_b64 exec, exec, s[6:7]
	v_rcp_f32_e32 v2, v88
	s_waitcnt lgkmcnt(0)
	v_mul_f32_e32 v18, v76, v2
	s_nop 1
	v_mov_b32_dpp v19, v18 quad_perm:[1,0,3,2] row_mask:0xf bank_mask:0xf bound_ctrl:1
	s_and_saveexec_b64 s[6:7], s[4:5]
	s_cbranch_execz .LBB0_635
	s_waitcnt lgkmcnt(0)
	v_cvt_pk_bf16_f32 v20, v18, v19
	v_add_co_u32_e32 v18, vcc, 0x9000, v16
	s_nop 1
	v_addc_co_u32_e32 v19, vcc, 0, v17, vcc
	global_store_dword v[18:19], v20, off
.LBB0_635:
	s_or_b64 exec, exec, s[6:7]
	v_mul_f32_e32 v18, v60, v2
	s_waitcnt lgkmcnt(0)
	s_nop 1
	v_mov_b32_dpp v19, v18 quad_perm:[1,0,3,2] row_mask:0xf bank_mask:0xf bound_ctrl:1
	s_and_saveexec_b64 s[6:7], s[4:5]
	s_cbranch_execz .LBB0_637
	s_waitcnt lgkmcnt(0)
	v_cvt_pk_bf16_f32 v20, v18, v19
	v_add_co_u32_e32 v18, vcc, 0x9000, v16
	s_nop 1
	v_addc_co_u32_e32 v19, vcc, 0, v17, vcc
	global_store_dword v[18:19], v20, off offset:64
.LBB0_637:
	s_or_b64 exec, exec, s[6:7]
	v_mul_f32_e32 v18, v44, v2
	s_waitcnt lgkmcnt(0)
	s_nop 1
	v_mov_b32_dpp v19, v18 quad_perm:[1,0,3,2] row_mask:0xf bank_mask:0xf bound_ctrl:1
	s_and_saveexec_b64 s[6:7], s[4:5]
	s_cbranch_execz .LBB0_639
	s_waitcnt lgkmcnt(0)
	v_cvt_pk_bf16_f32 v20, v18, v19
	v_add_co_u32_e32 v18, vcc, 0x9000, v16
	s_nop 1
	v_addc_co_u32_e32 v19, vcc, 0, v17, vcc
	global_store_dword v[18:19], v20, off offset:128
.LBB0_639:
	s_or_b64 exec, exec, s[6:7]
	v_mul_f32_e32 v2, v28, v2
	s_nop 1
	v_mov_b32_dpp v18, v2 quad_perm:[1,0,3,2] row_mask:0xf bank_mask:0xf bound_ctrl:1
	s_and_saveexec_b64 s[6:7], s[4:5]
	s_cbranch_execz .LBB0_641
	s_waitcnt lgkmcnt(0)
	v_cvt_pk_bf16_f32 v2, v2, v18
	v_add_co_u32_e32 v18, vcc, 0x9000, v16
	s_nop 1
	v_addc_co_u32_e32 v19, vcc, 0, v17, vcc
	global_store_dword v[18:19], v2, off offset:192
.LBB0_641:
	s_or_b64 exec, exec, s[6:7]
	v_rcp_f32_e32 v2, v89
	s_waitcnt lgkmcnt(0)
	v_mul_f32_e32 v18, v77, v2
	s_nop 1
	v_mov_b32_dpp v19, v18 quad_perm:[1,0,3,2] row_mask:0xf bank_mask:0xf bound_ctrl:1
	s_and_saveexec_b64 s[6:7], s[4:5]
	s_cbranch_execz .LBB0_643
	s_waitcnt lgkmcnt(0)
	v_cvt_pk_bf16_f32 v20, v18, v19
	v_add_co_u32_e32 v18, vcc, 0x9000, v16
	s_nop 1
	v_addc_co_u32_e32 v19, vcc, 0, v17, vcc
	global_store_dword v[18:19], v20, off offset:2048
.LBB0_643:
	s_or_b64 exec, exec, s[6:7]
	v_mul_f32_e32 v18, v61, v2
	s_waitcnt lgkmcnt(0)
	s_nop 1
	v_mov_b32_dpp v19, v18 quad_perm:[1,0,3,2] row_mask:0xf bank_mask:0xf bound_ctrl:1
	s_and_saveexec_b64 s[6:7], s[4:5]
	s_cbranch_execz .LBB0_645
	s_waitcnt lgkmcnt(0)
	v_cvt_pk_bf16_f32 v20, v18, v19
	v_add_co_u32_e32 v18, vcc, 0x9000, v16
	s_nop 1
	v_addc_co_u32_e32 v19, vcc, 0, v17, vcc
	global_store_dword v[18:19], v20, off offset:2112
.LBB0_645:
	s_or_b64 exec, exec, s[6:7]
	v_mul_f32_e32 v18, v45, v2
	s_waitcnt lgkmcnt(0)
	s_nop 1
	v_mov_b32_dpp v19, v18 quad_perm:[1,0,3,2] row_mask:0xf bank_mask:0xf bound_ctrl:1
	s_and_saveexec_b64 s[6:7], s[4:5]
	s_cbranch_execz .LBB0_647
	s_waitcnt lgkmcnt(0)
	v_cvt_pk_bf16_f32 v20, v18, v19
	v_add_co_u32_e32 v18, vcc, 0x9000, v16
	s_nop 1
	v_addc_co_u32_e32 v19, vcc, 0, v17, vcc
	global_store_dword v[18:19], v20, off offset:2176
.LBB0_647:
	s_or_b64 exec, exec, s[6:7]
	v_mul_f32_e32 v2, v29, v2
	s_nop 1
	v_mov_b32_dpp v18, v2 quad_perm:[1,0,3,2] row_mask:0xf bank_mask:0xf bound_ctrl:1
	s_and_saveexec_b64 s[6:7], s[4:5]
	s_cbranch_execz .LBB0_649
	s_waitcnt lgkmcnt(0)
	v_cvt_pk_bf16_f32 v2, v2, v18
	v_add_co_u32_e32 v18, vcc, 0x9000, v16
	s_nop 1
	v_addc_co_u32_e32 v19, vcc, 0, v17, vcc
	global_store_dword v[18:19], v2, off offset:2240
.LBB0_649:
	s_or_b64 exec, exec, s[6:7]
	v_rcp_f32_e32 v2, v82
	s_waitcnt lgkmcnt(0)
	v_mul_f32_e32 v18, v78, v2
	s_nop 1
	v_mov_b32_dpp v19, v18 quad_perm:[1,0,3,2] row_mask:0xf bank_mask:0xf bound_ctrl:1
	s_and_saveexec_b64 s[6:7], s[4:5]
	s_cbranch_execz .LBB0_651
	s_waitcnt lgkmcnt(0)
	v_cvt_pk_bf16_f32 v20, v18, v19
	v_add_co_u32_e32 v18, vcc, 0xc000, v16
	s_nop 1
	v_addc_co_u32_e32 v19, vcc, 0, v17, vcc
	global_store_dword v[18:19], v20, off
.LBB0_651:
	s_or_b64 exec, exec, s[6:7]
	v_mul_f32_e32 v18, v62, v2
	s_waitcnt lgkmcnt(0)
	s_nop 1
	v_mov_b32_dpp v19, v18 quad_perm:[1,0,3,2] row_mask:0xf bank_mask:0xf bound_ctrl:1
	s_and_saveexec_b64 s[6:7], s[4:5]
	s_cbranch_execz .LBB0_653
	s_waitcnt lgkmcnt(0)
	v_cvt_pk_bf16_f32 v20, v18, v19
	v_add_co_u32_e32 v18, vcc, 0xc000, v16
	s_nop 1
	v_addc_co_u32_e32 v19, vcc, 0, v17, vcc
	global_store_dword v[18:19], v20, off offset:64
.LBB0_653:
	s_or_b64 exec, exec, s[6:7]
	v_mul_f32_e32 v18, v46, v2
	s_waitcnt lgkmcnt(0)
	s_nop 1
	v_mov_b32_dpp v19, v18 quad_perm:[1,0,3,2] row_mask:0xf bank_mask:0xf bound_ctrl:1
	s_and_saveexec_b64 s[6:7], s[4:5]
	s_cbranch_execz .LBB0_655
	s_waitcnt lgkmcnt(0)
	v_cvt_pk_bf16_f32 v20, v18, v19
	v_add_co_u32_e32 v18, vcc, 0xc000, v16
	s_nop 1
	v_addc_co_u32_e32 v19, vcc, 0, v17, vcc
	global_store_dword v[18:19], v20, off offset:128
.LBB0_655:
	s_or_b64 exec, exec, s[6:7]
	v_mul_f32_e32 v2, v30, v2
	s_nop 1
	v_mov_b32_dpp v18, v2 quad_perm:[1,0,3,2] row_mask:0xf bank_mask:0xf bound_ctrl:1
	s_and_saveexec_b64 s[6:7], s[4:5]
	s_cbranch_execz .LBB0_657
	s_waitcnt lgkmcnt(0)
	v_cvt_pk_bf16_f32 v2, v2, v18
	v_add_co_u32_e32 v18, vcc, 0xc000, v16
	s_nop 1
	v_addc_co_u32_e32 v19, vcc, 0, v17, vcc
	global_store_dword v[18:19], v2, off offset:192
; __device__ __forceinline__ unsigned cvtpk(float lo, float hi) { unsigned r; asm volatile("v_cvt_pk_bf16_f32 %0, %1, %2" : "=v"(r) : "v"(lo), "v"(hi)); return r; }
; template <int MODE>
; __device__ __forceinline__ void attn_block_pipe(const BlockRef& cur, const BlockRef& nxt, char* lds, LAS unsigned char* ldsl, Seam<MODE>& S) {
;     ...
; #pragma unroll
;     for (int r = 0; r < 16; ++r) { const size_t ou_ = (size_t)((r & 3) + 8 * (r >> 2)) * cur.os;
; #pragma unroll
;         for (int d0 = 0; d0 < 4; ++d0) { const float v = o[d0][r] * rli[r];
;             const float vn = __shfl_xor(v, 1);
;             if ((r32 & 1) == 0) *(unsigned*)((char*)(Ow + ou_ + d0 * 32) + ol_) = cvtpk(v, vn); } }
.LBB0_657:
	s_or_b64 exec, exec, s[6:7]
	v_rcp_f32_e32 v2, v83
	s_waitcnt lgkmcnt(0)
	v_mul_f32_e32 v18, v79, v2
	s_nop 1
	v_mov_b32_dpp v19, v18 quad_perm:[1,0,3,2] row_mask:0xf bank_mask:0xf bound_ctrl:1
	s_and_saveexec_b64 s[6:7], s[4:5]
	s_cbranch_execz .LBB0_659
	s_waitcnt lgkmcnt(0)
	v_cvt_pk_bf16_f32 v20, v18, v19
	v_add_co_u32_e32 v18, vcc, 0xc000, v16
	s_nop 1
	v_addc_co_u32_e32 v19, vcc, 0, v17, vcc
	global_store_dword v[18:19], v20, off offset:2048
.LBB0_659:
	s_or_b64 exec, exec, s[6:7]
	v_mul_f32_e32 v18, v63, v2
	s_waitcnt lgkmcnt(0)
	s_nop 1
	v_mov_b32_dpp v19, v18 quad_perm:[1,0,3,2] row_mask:0xf bank_mask:0xf bound_ctrl:1
	s_and_saveexec_b64 s[6:7], s[4:5]
	s_cbranch_execz .LBB0_661
	s_waitcnt lgkmcnt(0)
	v_cvt_pk_bf16_f32 v20, v18, v19
	v_add_co_u32_e32 v18, vcc, 0xc000, v16
	s_nop 1
	v_addc_co_u32_e32 v19, vcc, 0, v17, vcc
	global_store_dword v[18:19], v20, off offset:2112
.LBB0_661:
	s_or_b64 exec, exec, s[6:7]
	v_mul_f32_e32 v18, v47, v2
	s_waitcnt lgkmcnt(0)
	s_nop 1
	v_mov_b32_dpp v19, v18 quad_perm:[1,0,3,2] row_mask:0xf bank_mask:0xf bound_ctrl:1
	s_and_saveexec_b64 s[6:7], s[4:5]
	s_cbranch_execz .LBB0_663
	s_waitcnt lgkmcnt(0)
	v_cvt_pk_bf16_f32 v20, v18, v19
	v_add_co_u32_e32 v18, vcc, 0xc000, v16
	s_nop 1
	v_addc_co_u32_e32 v19, vcc, 0, v17, vcc
	global_store_dword v[18:19], v20, off offset:2176
.LBB0_663:
	s_or_b64 exec, exec, s[6:7]
	v_mul_f32_e32 v2, v31, v2
	s_nop 1
	v_mov_b32_dpp v18, v2 quad_perm:[1,0,3,2] row_mask:0xf bank_mask:0xf bound_ctrl:1
	s_and_saveexec_b64 s[6:7], s[4:5]
	s_cbranch_execz .LBB0_665
	s_waitcnt lgkmcnt(0)
	v_cvt_pk_bf16_f32 v2, v2, v18
	v_add_co_u32_e32 v18, vcc, 0xc000, v16
	s_nop 1
	v_addc_co_u32_e32 v19, vcc, 0, v17, vcc
	global_store_dword v[18:19], v2, off offset:2240
.LBB0_665:
	s_or_b64 exec, exec, s[6:7]
	v_rcp_f32_e32 v2, v84
	s_waitcnt lgkmcnt(0)
	v_mul_f32_e32 v18, v80, v2
	s_nop 1
	v_mov_b32_dpp v19, v18 quad_perm:[1,0,3,2] row_mask:0xf bank_mask:0xf bound_ctrl:1
	s_and_saveexec_b64 s[6:7], s[4:5]
	s_cbranch_execz .LBB0_667
	s_waitcnt lgkmcnt(0)
	v_cvt_pk_bf16_f32 v20, v18, v19
	v_add_co_u32_e32 v18, vcc, 0xd000, v16
	s_nop 1
	v_addc_co_u32_e32 v19, vcc, 0, v17, vcc
	global_store_dword v[18:19], v20, off
.LBB0_667:
	s_or_b64 exec, exec, s[6:7]
	v_mul_f32_e32 v18, v64, v2
	s_waitcnt lgkmcnt(0)
	s_nop 1
	v_mov_b32_dpp v19, v18 quad_perm:[1,0,3,2] row_mask:0xf bank_mask:0xf bound_ctrl:1
	s_and_saveexec_b64 s[6:7], s[4:5]
	s_cbranch_execz .LBB0_669
	s_waitcnt lgkmcnt(0)
	v_cvt_pk_bf16_f32 v20, v18, v19
	v_add_co_u32_e32 v18, vcc, 0xd000, v16
	s_nop 1
	v_addc_co_u32_e32 v19, vcc, 0, v17, vcc
	global_store_dword v[18:19], v20, off offset:64
.LBB0_669:
	s_or_b64 exec, exec, s[6:7]
	v_mul_f32_e32 v18, v48, v2
	s_waitcnt lgkmcnt(0)
	s_nop 1
	v_mov_b32_dpp v19, v18 quad_perm:[1,0,3,2] row_mask:0xf bank_mask:0xf bound_ctrl:1
	s_and_saveexec_b64 s[6:7], s[4:5]
	s_cbranch_execz .LBB0_671
	s_waitcnt lgkmcnt(0)
	v_cvt_pk_bf16_f32 v20, v18, v19
	v_add_co_u32_e32 v18, vcc, 0xd000, v16
	s_nop 1
	v_addc_co_u32_e32 v19, vcc, 0, v17, vcc
	global_store_dword v[18:19], v20, off offset:128
.LBB0_671:
	s_or_b64 exec, exec, s[6:7]
	v_mul_f32_e32 v2, v32, v2
	s_nop 1
	v_mov_b32_dpp v18, v2 quad_perm:[1,0,3,2] row_mask:0xf bank_mask:0xf bound_ctrl:1
	s_and_saveexec_b64 s[6:7], s[4:5]
	s_cbranch_execz .LBB0_673
	s_waitcnt lgkmcnt(0)
	v_cvt_pk_bf16_f32 v2, v2, v18
	v_add_co_u32_e32 v18, vcc, 0xd000, v16
	s_nop 1
	v_addc_co_u32_e32 v19, vcc, 0, v17, vcc
	global_store_dword v[18:19], v2, off offset:192
.LBB0_673:
	s_or_b64 exec, exec, s[6:7]
	v_rcp_f32_e32 v2, v85
	s_waitcnt lgkmcnt(0)
	v_mul_f32_e32 v18, v81, v2
	s_nop 1
	v_mov_b32_dpp v19, v18 quad_perm:[1,0,3,2] row_mask:0xf bank_mask:0xf bound_ctrl:1
	s_and_saveexec_b64 s[6:7], s[4:5]
	s_cbranch_execz .LBB0_675
	s_waitcnt lgkmcnt(0)
	v_cvt_pk_bf16_f32 v20, v18, v19
	v_add_co_u32_e32 v18, vcc, 0xd000, v16
	s_nop 1
	v_addc_co_u32_e32 v19, vcc, 0, v17, vcc
	global_store_dword v[18:19], v20, off offset:2048
.LBB0_675:
	s_or_b64 exec, exec, s[6:7]
	v_mul_f32_e32 v18, v65, v2
	s_waitcnt lgkmcnt(0)
	s_nop 1
	v_mov_b32_dpp v19, v18 quad_perm:[1,0,3,2] row_mask:0xf bank_mask:0xf bound_ctrl:1
	s_and_saveexec_b64 s[6:7], s[4:5]
	s_cbranch_execz .LBB0_677
	s_waitcnt lgkmcnt(0)
	v_cvt_pk_bf16_f32 v20, v18, v19
	v_add_co_u32_e32 v18, vcc, 0xd000, v16
	s_nop 1
	v_addc_co_u32_e32 v19, vcc, 0, v17, vcc
	global_store_dword v[18:19], v20, off offset:2112
.LBB0_677:
	s_or_b64 exec, exec, s[6:7]
	v_mul_f32_e32 v18, v49, v2
	s_waitcnt lgkmcnt(0)
	s_nop 1
	v_mov_b32_dpp v19, v18 quad_perm:[1,0,3,2] row_mask:0xf bank_mask:0xf bound_ctrl:1
	s_and_saveexec_b64 s[6:7], s[4:5]
	s_cbranch_execz .LBB0_679
	s_waitcnt lgkmcnt(0)
	v_cvt_pk_bf16_f32 v20, v18, v19
	v_add_co_u32_e32 v18, vcc, 0xd000, v16
	s_nop 1
	v_addc_co_u32_e32 v19, vcc, 0, v17, vcc
	global_store_dword v[18:19], v20, off offset:2176
.LBB0_679:
	s_or_b64 exec, exec, s[6:7]
	v_mul_f32_e32 v2, v33, v2
	s_nop 1
	v_mov_b32_dpp v18, v2 quad_perm:[1,0,3,2] row_mask:0xf bank_mask:0xf bound_ctrl:1
	s_and_saveexec_b64 s[6:7], s[4:5]
	s_cbranch_execz .LBB0_508
	v_add_co_u32_e32 v16, vcc, 0xd000, v16
	s_waitcnt lgkmcnt(0)
	v_cvt_pk_bf16_f32 v2, v2, v18
	s_nop 0
	v_addc_co_u32_e32 v17, vcc, 0, v17, vcc
	global_store_dword v[16:17], v2, off offset:2240
	s_branch .LBB0_508

; __device__ __forceinline__ int crow(int r, int hi) { return (r & 3) + 8 * (r >> 2) + 4 * hi; }
; __device__ __forceinline__ unsigned cvtpk(float lo, float hi) { unsigned r; asm volatile("v_cvt_pk_bf16_f32 %0, %1, %2" : "=v"(r) : "v"(lo), "v"(hi)); return r; }
; template <int MODE>
; __device__ __forceinline__ void attn_block_pipe(const BlockRef& cur, const BlockRef& nxt, char* lds, LAS unsigned char* ldsl, Seam<MODE>& S) {
;     ...
;     float rli[16];
; #pragma unroll
;     for (int r = 0; r < 16; ++r) rli[r] = __builtin_amdgcn_rcpf(li_l[crow(r, hi)]);
;     bf16_t* Ow = cur.O + (size_t)qlo * cur.os;
;     const unsigned ol_ = (unsigned)(4 * hi * cur.os + r32) * 2u;
; #pragma unroll
;     for (int r = 0; r < 16; ++r) { const size_t ou_ = (size_t)((r & 3) + 8 * (r >> 2)) * cur.os;
; #pragma unroll
;         for (int d0 = 0; d0 < 4; ++d0) { const float v = o[d0][r] * rli[r];
;             const float vn = __shfl_xor(v, 1);
;             if ((r32 & 1) == 0) *(unsigned*)((char*)(Ow + ou_ + d0 * 32) + ol_) = cvtpk(v, vn); } }
.LBB0_810:
	s_or_b64 exec, exec, s[4:5]
	ds_read_b128 v[110:113], v217
	ds_read_b128 v[106:109], v217 offset:32
	ds_read_b128 v[102:105], v217 offset:64
	ds_read_b128 v[98:101], v217 offset:96
	v_mul_lo_u32 v1, v216, s22
	s_waitcnt lgkmcnt(0)
	v_rcp_f32_e32 v19, v110
	v_and_b32_e32 v16, 64, v208
	v_or_b32_e32 v2, v1, v214
	v_xor_b32_e32 v1, 1, v208
	v_add_u32_e32 v16, 64, v16
	v_cmp_lt_i32_e32 vcc, v1, v16
	s_ashr_i32 s4, s89, 31
	s_mul_hi_u32 s5, s89, s22
	v_cndmask_b32_e32 v1, v208, v1, vcc
	s_mul_i32 s4, s4, s22
	v_lshlrev_b32_e32 v1, 2, v1
	v_mul_f32_e32 v32, v82, v19
	s_add_i32 s5, s5, s4
	s_mul_i32 s4, s89, s22
	s_nop 1
	v_mov_b32_dpp v33, v32 quad_perm:[1,0,3,2] row_mask:0xf bank_mask:0xf bound_ctrl:1
	s_lshl_b64 s[4:5], s[4:5], 1
	s_add_u32 s4, s50, s4
	s_addc_u32 s5, s51, s5
	v_lshlrev_b32_e32 v2, 1, v2
	v_and_b32_e32 v16, 1, v213
	v_cmp_eq_u32_e32 vcc, 0, v16
	v_lshl_add_u64 v[16:17], s[4:5], 0, v[2:3]
	s_and_saveexec_b64 s[4:5], vcc
	s_cbranch_execz .LBB0_812
	s_waitcnt lgkmcnt(0)
	v_cvt_pk_bf16_f32 v2, v32, v33
	global_store_dword v[16:17], v2, off
.LBB0_812:
	s_or_b64 exec, exec, s[4:5]
	v_mul_f32_e32 v2, v66, v19
	s_nop 1
	v_mov_b32_dpp v32, v2 quad_perm:[1,0,3,2] row_mask:0xf bank_mask:0xf bound_ctrl:1
	s_and_saveexec_b64 s[4:5], vcc
	s_cbranch_execz .LBB0_814
	s_waitcnt lgkmcnt(0)
	v_cvt_pk_bf16_f32 v2, v2, v32
	global_store_dword v[16:17], v2, off offset:64
.LBB0_814:
	s_or_b64 exec, exec, s[4:5]
	v_mul_f32_e32 v2, v50, v19
	s_waitcnt lgkmcnt(0)
	s_nop 1
	v_mov_b32_dpp v32, v2 quad_perm:[1,0,3,2] row_mask:0xf bank_mask:0xf bound_ctrl:1
	s_and_saveexec_b64 s[4:5], vcc
	s_cbranch_execz .LBB0_816
	s_waitcnt lgkmcnt(0)
	v_cvt_pk_bf16_f32 v2, v2, v32
	global_store_dword v[16:17], v2, off offset:128
.LBB0_816:
	s_or_b64 exec, exec, s[4:5]
	v_mul_f32_e32 v2, v34, v19
	s_nop 1
	v_mov_b32_dpp v19, v2 quad_perm:[1,0,3,2] row_mask:0xf bank_mask:0xf bound_ctrl:1
	s_and_saveexec_b64 s[4:5], vcc
	s_cbranch_execz .LBB0_818
	s_waitcnt lgkmcnt(0)
	v_cvt_pk_bf16_f32 v2, v2, v19
	global_store_dword v[16:17], v2, off offset:192
.LBB0_818:
	s_or_b64 exec, exec, s[4:5]
	v_rcp_f32_e32 v2, v111
	v_lshl_add_u64 v[16:17], s[22:23], 1, v[16:17]
	s_waitcnt lgkmcnt(0)
	v_mul_f32_e32 v19, v83, v2
	s_nop 1
	v_mov_b32_dpp v32, v19 quad_perm:[1,0,3,2] row_mask:0xf bank_mask:0xf bound_ctrl:1
	s_and_saveexec_b64 s[4:5], vcc
	s_cbranch_execz .LBB0_820
	s_waitcnt lgkmcnt(0)
	v_cvt_pk_bf16_f32 v19, v19, v32
	global_store_dword v[16:17], v19, off
.LBB0_820:
	s_or_b64 exec, exec, s[4:5]
	v_mul_f32_e32 v19, v67, v2
	s_waitcnt lgkmcnt(0)
	s_nop 1
	v_mov_b32_dpp v32, v19 quad_perm:[1,0,3,2] row_mask:0xf bank_mask:0xf bound_ctrl:1
	s_and_saveexec_b64 s[4:5], vcc
	s_cbranch_execz .LBB0_822
	s_waitcnt lgkmcnt(0)
	v_cvt_pk_bf16_f32 v19, v19, v32
	global_store_dword v[16:17], v19, off offset:64
.LBB0_822:
	s_or_b64 exec, exec, s[4:5]
	v_mul_f32_e32 v19, v51, v2
	s_waitcnt lgkmcnt(0)
	s_nop 1
	v_mov_b32_dpp v32, v19 quad_perm:[1,0,3,2] row_mask:0xf bank_mask:0xf bound_ctrl:1
	s_and_saveexec_b64 s[4:5], vcc
	s_cbranch_execz .LBB0_824
	s_waitcnt lgkmcnt(0)
	v_cvt_pk_bf16_f32 v19, v19, v32
	global_store_dword v[16:17], v19, off offset:128
.LBB0_824:
	s_or_b64 exec, exec, s[4:5]
	v_mul_f32_e32 v2, v35, v2
	s_nop 1
	v_mov_b32_dpp v19, v2 quad_perm:[1,0,3,2] row_mask:0xf bank_mask:0xf bound_ctrl:1
	s_and_saveexec_b64 s[4:5], vcc
	s_cbranch_execz .LBB0_826
	s_waitcnt lgkmcnt(0)
	v_cvt_pk_bf16_f32 v2, v2, v19
	global_store_dword v[16:17], v2, off offset:192
.LBB0_826:
	s_or_b64 exec, exec, s[4:5]
	v_rcp_f32_e32 v2, v112
	s_lshl_b64 s[4:5], s[22:23], 1
	v_lshl_add_u64 v[16:17], v[16:17], 0, s[4:5]
	s_waitcnt lgkmcnt(0)
	v_mul_f32_e32 v19, v84, v2
	s_nop 1
	v_mov_b32_dpp v32, v19 quad_perm:[1,0,3,2] row_mask:0xf bank_mask:0xf bound_ctrl:1
	s_and_saveexec_b64 s[6:7], vcc
	s_cbranch_execz .LBB0_828
	s_waitcnt lgkmcnt(0)
	v_cvt_pk_bf16_f32 v19, v19, v32
	global_store_dword v[16:17], v19, off
.LBB0_828:
	s_or_b64 exec, exec, s[6:7]
	v_mul_f32_e32 v19, v68, v2
	s_waitcnt lgkmcnt(0)
	s_nop 1
	v_mov_b32_dpp v32, v19 quad_perm:[1,0,3,2] row_mask:0xf bank_mask:0xf bound_ctrl:1
	s_and_saveexec_b64 s[6:7], vcc
	s_cbranch_execz .LBB0_830
	s_waitcnt lgkmcnt(0)
	v_cvt_pk_bf16_f32 v19, v19, v32
	global_store_dword v[16:17], v19, off offset:64
.LBB0_830:
	s_or_b64 exec, exec, s[6:7]
	v_mul_f32_e32 v19, v52, v2
	s_waitcnt lgkmcnt(0)
	s_nop 1
	v_mov_b32_dpp v32, v19 quad_perm:[1,0,3,2] row_mask:0xf bank_mask:0xf bound_ctrl:1
	s_and_saveexec_b64 s[6:7], vcc
	s_cbranch_execz .LBB0_832
	s_waitcnt lgkmcnt(0)
	v_cvt_pk_bf16_f32 v19, v19, v32
	global_store_dword v[16:17], v19, off offset:128
.LBB0_832:
	s_or_b64 exec, exec, s[6:7]
	v_mul_f32_e32 v2, v36, v2
	s_nop 1
	v_mov_b32_dpp v19, v2 quad_perm:[1,0,3,2] row_mask:0xf bank_mask:0xf bound_ctrl:1
	s_and_saveexec_b64 s[6:7], vcc
	s_cbranch_execz .LBB0_834
	s_waitcnt lgkmcnt(0)
	v_cvt_pk_bf16_f32 v2, v2, v19
	global_store_dword v[16:17], v2, off offset:192
.LBB0_834:
	s_or_b64 exec, exec, s[6:7]
	v_rcp_f32_e32 v2, v113
	v_lshl_add_u64 v[16:17], v[16:17], 0, s[4:5]
	s_waitcnt lgkmcnt(0)
	v_mul_f32_e32 v19, v85, v2
	s_nop 1
	v_mov_b32_dpp v32, v19 quad_perm:[1,0,3,2] row_mask:0xf bank_mask:0xf bound_ctrl:1
	s_and_saveexec_b64 s[6:7], vcc
	s_cbranch_execz .LBB0_836
	s_waitcnt lgkmcnt(0)
	v_cvt_pk_bf16_f32 v19, v19, v32
	global_store_dword v[16:17], v19, off
.LBB0_836:
	s_or_b64 exec, exec, s[6:7]
	v_mul_f32_e32 v19, v69, v2
	s_waitcnt lgkmcnt(0)
	s_nop 1
	v_mov_b32_dpp v32, v19 quad_perm:[1,0,3,2] row_mask:0xf bank_mask:0xf bound_ctrl:1
	s_and_saveexec_b64 s[6:7], vcc
	s_cbranch_execz .LBB0_838
	s_waitcnt lgkmcnt(0)
	v_cvt_pk_bf16_f32 v19, v19, v32
	global_store_dword v[16:17], v19, off offset:64
; __device__ __forceinline__ unsigned cvtpk(float lo, float hi) { unsigned r; asm volatile("v_cvt_pk_bf16_f32 %0, %1, %2" : "=v"(r) : "v"(lo), "v"(hi)); return r; }
; template <int MODE>
; __device__ __forceinline__ void attn_block_pipe(const BlockRef& cur, const BlockRef& nxt, char* lds, LAS unsigned char* ldsl, Seam<MODE>& S) {
;     ...
; #pragma unroll
;     for (int r = 0; r < 16; ++r) { const size_t ou_ = (size_t)((r & 3) + 8 * (r >> 2)) * cur.os;
; #pragma unroll
;         for (int d0 = 0; d0 < 4; ++d0) { const float v = o[d0][r] * rli[r];
;             const float vn = __shfl_xor(v, 1);
;             if ((r32 & 1) == 0) *(unsigned*)((char*)(Ow + ou_ + d0 * 32) + ol_) = cvtpk(v, vn); } }
.LBB0_838:
	s_or_b64 exec, exec, s[6:7]
	v_mul_f32_e32 v19, v53, v2
	s_waitcnt lgkmcnt(0)
	s_nop 1
	v_mov_b32_dpp v32, v19 quad_perm:[1,0,3,2] row_mask:0xf bank_mask:0xf bound_ctrl:1
	s_and_saveexec_b64 s[6:7], vcc
	s_cbranch_execz .LBB0_840
	s_waitcnt lgkmcnt(0)
	v_cvt_pk_bf16_f32 v19, v19, v32
	global_store_dword v[16:17], v19, off offset:128
.LBB0_840:
	s_or_b64 exec, exec, s[6:7]
	v_mul_f32_e32 v2, v37, v2
	s_nop 1
	v_mov_b32_dpp v19, v2 quad_perm:[1,0,3,2] row_mask:0xf bank_mask:0xf bound_ctrl:1
	s_and_saveexec_b64 s[6:7], vcc
	s_cbranch_execz .LBB0_842
	s_waitcnt lgkmcnt(0)
	v_cvt_pk_bf16_f32 v2, v2, v19
	global_store_dword v[16:17], v2, off offset:192
.LBB0_842:
	s_or_b64 exec, exec, s[6:7]
	v_rcp_f32_e32 v2, v106
	v_mad_u64_u32 v[16:17], s[6:7], s22, 10, v[16:17]
	s_waitcnt lgkmcnt(0)
	v_mul_f32_e32 v19, v86, v2
	s_nop 1
	v_mov_b32_dpp v32, v19 quad_perm:[1,0,3,2] row_mask:0xf bank_mask:0xf bound_ctrl:1
	s_and_saveexec_b64 s[6:7], vcc
	s_cbranch_execz .LBB0_844
	s_waitcnt lgkmcnt(0)
	v_cvt_pk_bf16_f32 v19, v19, v32
	global_store_dword v[16:17], v19, off
.LBB0_844:
	s_or_b64 exec, exec, s[6:7]
	v_mul_f32_e32 v19, v70, v2
	s_waitcnt lgkmcnt(0)
	s_nop 1
	v_mov_b32_dpp v32, v19 quad_perm:[1,0,3,2] row_mask:0xf bank_mask:0xf bound_ctrl:1
	s_and_saveexec_b64 s[6:7], vcc
	s_cbranch_execz .LBB0_846
	s_waitcnt lgkmcnt(0)
	v_cvt_pk_bf16_f32 v19, v19, v32
	global_store_dword v[16:17], v19, off offset:64
.LBB0_846:
	s_or_b64 exec, exec, s[6:7]
	v_mul_f32_e32 v19, v54, v2
	s_waitcnt lgkmcnt(0)
	s_nop 1
	v_mov_b32_dpp v32, v19 quad_perm:[1,0,3,2] row_mask:0xf bank_mask:0xf bound_ctrl:1
	s_and_saveexec_b64 s[6:7], vcc
	s_cbranch_execz .LBB0_848
	s_waitcnt lgkmcnt(0)
	v_cvt_pk_bf16_f32 v19, v19, v32
	global_store_dword v[16:17], v19, off offset:128
.LBB0_848:
	s_or_b64 exec, exec, s[6:7]
	v_mul_f32_e32 v2, v38, v2
	s_nop 1
	v_mov_b32_dpp v19, v2 quad_perm:[1,0,3,2] row_mask:0xf bank_mask:0xf bound_ctrl:1
	s_and_saveexec_b64 s[6:7], vcc
	s_cbranch_execz .LBB0_850
	s_waitcnt lgkmcnt(0)
	v_cvt_pk_bf16_f32 v2, v2, v19
	global_store_dword v[16:17], v2, off offset:192
.LBB0_850:
	s_or_b64 exec, exec, s[6:7]
	v_rcp_f32_e32 v2, v107
	v_lshl_add_u64 v[16:17], v[16:17], 0, s[4:5]
	s_waitcnt lgkmcnt(0)
	v_mul_f32_e32 v19, v87, v2
	s_nop 1
	v_mov_b32_dpp v32, v19 quad_perm:[1,0,3,2] row_mask:0xf bank_mask:0xf bound_ctrl:1
	s_and_saveexec_b64 s[6:7], vcc
	s_cbranch_execz .LBB0_852
	s_waitcnt lgkmcnt(0)
	v_cvt_pk_bf16_f32 v19, v19, v32
	global_store_dword v[16:17], v19, off
.LBB0_852:
	s_or_b64 exec, exec, s[6:7]
	v_mul_f32_e32 v19, v71, v2
	s_waitcnt lgkmcnt(0)
	s_nop 1
	v_mov_b32_dpp v32, v19 quad_perm:[1,0,3,2] row_mask:0xf bank_mask:0xf bound_ctrl:1
	s_and_saveexec_b64 s[6:7], vcc
	s_cbranch_execz .LBB0_854
	s_waitcnt lgkmcnt(0)
	v_cvt_pk_bf16_f32 v19, v19, v32
	global_store_dword v[16:17], v19, off offset:64
.LBB0_854:
	s_or_b64 exec, exec, s[6:7]
	v_mul_f32_e32 v19, v55, v2
	s_waitcnt lgkmcnt(0)
	s_nop 1
	v_mov_b32_dpp v32, v19 quad_perm:[1,0,3,2] row_mask:0xf bank_mask:0xf bound_ctrl:1
	s_and_saveexec_b64 s[6:7], vcc
	s_cbranch_execz .LBB0_856
	s_waitcnt lgkmcnt(0)
	v_cvt_pk_bf16_f32 v19, v19, v32
	global_store_dword v[16:17], v19, off offset:128
.LBB0_856:
	s_or_b64 exec, exec, s[6:7]
	v_mul_f32_e32 v2, v39, v2
	s_nop 1
	v_mov_b32_dpp v19, v2 quad_perm:[1,0,3,2] row_mask:0xf bank_mask:0xf bound_ctrl:1
	s_and_saveexec_b64 s[6:7], vcc
	s_cbranch_execz .LBB0_858
	s_waitcnt lgkmcnt(0)
	v_cvt_pk_bf16_f32 v2, v2, v19
	global_store_dword v[16:17], v2, off offset:192
.LBB0_858:
	s_or_b64 exec, exec, s[6:7]
	v_rcp_f32_e32 v2, v108
	v_lshl_add_u64 v[16:17], v[16:17], 0, s[4:5]
	s_waitcnt lgkmcnt(0)
	v_mul_f32_e32 v19, v88, v2
	s_nop 1
	v_mov_b32_dpp v32, v19 quad_perm:[1,0,3,2] row_mask:0xf bank_mask:0xf bound_ctrl:1
	s_and_saveexec_b64 s[6:7], vcc
	s_cbranch_execz .LBB0_860
	s_waitcnt lgkmcnt(0)
	v_cvt_pk_bf16_f32 v19, v19, v32
	global_store_dword v[16:17], v19, off
.LBB0_860:
	s_or_b64 exec, exec, s[6:7]
	v_mul_f32_e32 v19, v72, v2
	s_waitcnt lgkmcnt(0)
	s_nop 1
	v_mov_b32_dpp v32, v19 quad_perm:[1,0,3,2] row_mask:0xf bank_mask:0xf bound_ctrl:1
	s_and_saveexec_b64 s[6:7], vcc
	s_cbranch_execz .LBB0_862
	s_waitcnt lgkmcnt(0)
	v_cvt_pk_bf16_f32 v19, v19, v32
	global_store_dword v[16:17], v19, off offset:64
.LBB0_862:
	s_or_b64 exec, exec, s[6:7]
	v_mul_f32_e32 v19, v56, v2
	s_waitcnt lgkmcnt(0)
	s_nop 1
	v_mov_b32_dpp v32, v19 quad_perm:[1,0,3,2] row_mask:0xf bank_mask:0xf bound_ctrl:1
	s_and_saveexec_b64 s[6:7], vcc
	s_cbranch_execz .LBB0_864
	s_waitcnt lgkmcnt(0)
	v_cvt_pk_bf16_f32 v19, v19, v32
	global_store_dword v[16:17], v19, off offset:128
.LBB0_864:
	s_or_b64 exec, exec, s[6:7]
	v_mul_f32_e32 v2, v40, v2
	s_nop 1
	v_mov_b32_dpp v19, v2 quad_perm:[1,0,3,2] row_mask:0xf bank_mask:0xf bound_ctrl:1
	s_and_saveexec_b64 s[6:7], vcc
	s_cbranch_execz .LBB0_866
	s_waitcnt lgkmcnt(0)
	v_cvt_pk_bf16_f32 v2, v2, v19
	global_store_dword v[16:17], v2, off offset:192
.LBB0_866:
	s_or_b64 exec, exec, s[6:7]
	v_rcp_f32_e32 v2, v109
	v_lshl_add_u64 v[16:17], v[16:17], 0, s[4:5]
	s_waitcnt lgkmcnt(0)
	v_mul_f32_e32 v19, v89, v2
	s_nop 1
	v_mov_b32_dpp v32, v19 quad_perm:[1,0,3,2] row_mask:0xf bank_mask:0xf bound_ctrl:1
	s_and_saveexec_b64 s[6:7], vcc
	s_cbranch_execz .LBB0_868
	s_waitcnt lgkmcnt(0)
	v_cvt_pk_bf16_f32 v19, v19, v32
	global_store_dword v[16:17], v19, off
.LBB0_868:
	s_or_b64 exec, exec, s[6:7]
	v_mul_f32_e32 v19, v73, v2
	s_waitcnt lgkmcnt(0)
	s_nop 1
	v_mov_b32_dpp v32, v19 quad_perm:[1,0,3,2] row_mask:0xf bank_mask:0xf bound_ctrl:1
	s_and_saveexec_b64 s[6:7], vcc
	s_cbranch_execz .LBB0_870
	s_waitcnt lgkmcnt(0)
	v_cvt_pk_bf16_f32 v19, v19, v32
	global_store_dword v[16:17], v19, off offset:64
; __device__ __forceinline__ unsigned cvtpk(float lo, float hi) { unsigned r; asm volatile("v_cvt_pk_bf16_f32 %0, %1, %2" : "=v"(r) : "v"(lo), "v"(hi)); return r; }
; template <int MODE>
; __device__ __forceinline__ void attn_block_pipe(const BlockRef& cur, const BlockRef& nxt, char* lds, LAS unsigned char* ldsl, Seam<MODE>& S) {
;     ...
; #pragma unroll
;     for (int r = 0; r < 16; ++r) { const size_t ou_ = (size_t)((r & 3) + 8 * (r >> 2)) * cur.os;
; #pragma unroll
;         for (int d0 = 0; d0 < 4; ++d0) { const float v = o[d0][r] * rli[r];
;             const float vn = __shfl_xor(v, 1);
;             if ((r32 & 1) == 0) *(unsigned*)((char*)(Ow + ou_ + d0 * 32) + ol_) = cvtpk(v, vn); } }
.LBB0_870:
	s_or_b64 exec, exec, s[6:7]
	v_mul_f32_e32 v19, v57, v2
	s_waitcnt lgkmcnt(0)
	s_nop 1
	v_mov_b32_dpp v32, v19 quad_perm:[1,0,3,2] row_mask:0xf bank_mask:0xf bound_ctrl:1
	s_and_saveexec_b64 s[6:7], vcc
	s_cbranch_execz .LBB0_872
	s_waitcnt lgkmcnt(0)
	v_cvt_pk_bf16_f32 v19, v19, v32
	global_store_dword v[16:17], v19, off offset:128
.LBB0_872:
	s_or_b64 exec, exec, s[6:7]
	v_mul_f32_e32 v2, v41, v2
	s_nop 1
	v_mov_b32_dpp v19, v2 quad_perm:[1,0,3,2] row_mask:0xf bank_mask:0xf bound_ctrl:1
	s_and_saveexec_b64 s[6:7], vcc
	s_cbranch_execz .LBB0_874
	s_waitcnt lgkmcnt(0)
	v_cvt_pk_bf16_f32 v2, v2, v19
	global_store_dword v[16:17], v2, off offset:192
.LBB0_874:
	s_or_b64 exec, exec, s[6:7]
	v_rcp_f32_e32 v2, v102
	s_mul_hi_u32 s7, s22, 10
	s_mul_i32 s6, s22, 10
	v_lshl_add_u64 v[16:17], v[16:17], 0, s[6:7]
	s_waitcnt lgkmcnt(0)
	v_mul_f32_e32 v19, v90, v2
	s_nop 1
	v_mov_b32_dpp v32, v19 quad_perm:[1,0,3,2] row_mask:0xf bank_mask:0xf bound_ctrl:1
	s_and_saveexec_b64 s[8:9], vcc
	s_cbranch_execz .LBB0_876
	s_waitcnt lgkmcnt(0)
	v_cvt_pk_bf16_f32 v19, v19, v32
	global_store_dword v[16:17], v19, off
.LBB0_876:
	s_or_b64 exec, exec, s[8:9]
	v_mul_f32_e32 v19, v74, v2
	s_waitcnt lgkmcnt(0)
	s_nop 1
	v_mov_b32_dpp v32, v19 quad_perm:[1,0,3,2] row_mask:0xf bank_mask:0xf bound_ctrl:1
	s_and_saveexec_b64 s[8:9], vcc
	s_cbranch_execz .LBB0_878
	s_waitcnt lgkmcnt(0)
	v_cvt_pk_bf16_f32 v19, v19, v32
	global_store_dword v[16:17], v19, off offset:64
.LBB0_878:
	s_or_b64 exec, exec, s[8:9]
	v_mul_f32_e32 v19, v58, v2
	s_waitcnt lgkmcnt(0)
	s_nop 1
	v_mov_b32_dpp v32, v19 quad_perm:[1,0,3,2] row_mask:0xf bank_mask:0xf bound_ctrl:1
	s_and_saveexec_b64 s[8:9], vcc
	s_cbranch_execz .LBB0_880
	s_waitcnt lgkmcnt(0)
	v_cvt_pk_bf16_f32 v19, v19, v32
	global_store_dword v[16:17], v19, off offset:128
.LBB0_880:
	s_or_b64 exec, exec, s[8:9]
	v_mul_f32_e32 v2, v42, v2
	s_nop 1
	v_mov_b32_dpp v19, v2 quad_perm:[1,0,3,2] row_mask:0xf bank_mask:0xf bound_ctrl:1
	s_and_saveexec_b64 s[8:9], vcc
	s_cbranch_execz .LBB0_882
	s_waitcnt lgkmcnt(0)
	v_cvt_pk_bf16_f32 v2, v2, v19
	global_store_dword v[16:17], v2, off offset:192
.LBB0_882:
	s_or_b64 exec, exec, s[8:9]
	v_rcp_f32_e32 v2, v103
	v_lshl_add_u64 v[16:17], v[16:17], 0, s[4:5]
	s_waitcnt lgkmcnt(0)
	v_mul_f32_e32 v19, v91, v2
	s_nop 1
	v_mov_b32_dpp v32, v19 quad_perm:[1,0,3,2] row_mask:0xf bank_mask:0xf bound_ctrl:1
	s_and_saveexec_b64 s[8:9], vcc
	s_cbranch_execz .LBB0_884
	s_waitcnt lgkmcnt(0)
	v_cvt_pk_bf16_f32 v19, v19, v32
	global_store_dword v[16:17], v19, off
.LBB0_884:
	s_or_b64 exec, exec, s[8:9]
	v_mul_f32_e32 v19, v75, v2
	s_waitcnt lgkmcnt(0)
	s_nop 1
	v_mov_b32_dpp v32, v19 quad_perm:[1,0,3,2] row_mask:0xf bank_mask:0xf bound_ctrl:1
	s_and_saveexec_b64 s[8:9], vcc
	s_cbranch_execz .LBB0_886
	s_waitcnt lgkmcnt(0)
	v_cvt_pk_bf16_f32 v19, v19, v32
	global_store_dword v[16:17], v19, off offset:64
.LBB0_886:
	s_or_b64 exec, exec, s[8:9]
	v_mul_f32_e32 v19, v59, v2
	s_waitcnt lgkmcnt(0)
	s_nop 1
	v_mov_b32_dpp v32, v19 quad_perm:[1,0,3,2] row_mask:0xf bank_mask:0xf bound_ctrl:1
	s_and_saveexec_b64 s[8:9], vcc
	s_cbranch_execz .LBB0_888
	s_waitcnt lgkmcnt(0)
	v_cvt_pk_bf16_f32 v19, v19, v32
	global_store_dword v[16:17], v19, off offset:128
.LBB0_888:
	s_or_b64 exec, exec, s[8:9]
	v_mul_f32_e32 v2, v43, v2
	s_nop 1
	v_mov_b32_dpp v19, v2 quad_perm:[1,0,3,2] row_mask:0xf bank_mask:0xf bound_ctrl:1
	s_and_saveexec_b64 s[8:9], vcc
	s_cbranch_execz .LBB0_890
	s_waitcnt lgkmcnt(0)
	v_cvt_pk_bf16_f32 v2, v2, v19
	global_store_dword v[16:17], v2, off offset:192
.LBB0_890:
	s_or_b64 exec, exec, s[8:9]
	v_rcp_f32_e32 v2, v104
	v_lshl_add_u64 v[16:17], v[16:17], 0, s[4:5]
	s_waitcnt lgkmcnt(0)
	v_mul_f32_e32 v19, v92, v2
	s_nop 1
	v_mov_b32_dpp v32, v19 quad_perm:[1,0,3,2] row_mask:0xf bank_mask:0xf bound_ctrl:1
	s_and_saveexec_b64 s[8:9], vcc
	s_cbranch_execz .LBB0_892
	s_waitcnt lgkmcnt(0)
	v_cvt_pk_bf16_f32 v19, v19, v32
	global_store_dword v[16:17], v19, off
.LBB0_892:
	s_or_b64 exec, exec, s[8:9]
	v_mul_f32_e32 v19, v76, v2
	s_waitcnt lgkmcnt(0)
	s_nop 1
	v_mov_b32_dpp v32, v19 quad_perm:[1,0,3,2] row_mask:0xf bank_mask:0xf bound_ctrl:1
	s_and_saveexec_b64 s[8:9], vcc
	s_cbranch_execz .LBB0_894
	s_waitcnt lgkmcnt(0)
	v_cvt_pk_bf16_f32 v19, v19, v32
	global_store_dword v[16:17], v19, off offset:64
.LBB0_894:
	s_or_b64 exec, exec, s[8:9]
	v_mul_f32_e32 v19, v60, v2
	s_waitcnt lgkmcnt(0)
	s_nop 1
	v_mov_b32_dpp v32, v19 quad_perm:[1,0,3,2] row_mask:0xf bank_mask:0xf bound_ctrl:1
	s_and_saveexec_b64 s[8:9], vcc
	s_cbranch_execz .LBB0_896
	s_waitcnt lgkmcnt(0)
	v_cvt_pk_bf16_f32 v19, v19, v32
	global_store_dword v[16:17], v19, off offset:128
.LBB0_896:
	s_or_b64 exec, exec, s[8:9]
	v_mul_f32_e32 v2, v44, v2
	s_nop 1
	v_mov_b32_dpp v19, v2 quad_perm:[1,0,3,2] row_mask:0xf bank_mask:0xf bound_ctrl:1
	s_and_saveexec_b64 s[8:9], vcc
	s_cbranch_execz .LBB0_898
	s_waitcnt lgkmcnt(0)
	v_cvt_pk_bf16_f32 v2, v2, v19
	global_store_dword v[16:17], v2, off offset:192
.LBB0_898:
	s_or_b64 exec, exec, s[8:9]
	v_rcp_f32_e32 v2, v105
	v_lshl_add_u64 v[16:17], v[16:17], 0, s[4:5]
	s_waitcnt lgkmcnt(0)
	v_mul_f32_e32 v19, v93, v2
	s_nop 1
	v_mov_b32_dpp v32, v19 quad_perm:[1,0,3,2] row_mask:0xf bank_mask:0xf bound_ctrl:1
	s_and_saveexec_b64 s[8:9], vcc
	s_cbranch_execz .LBB0_900
	s_waitcnt lgkmcnt(0)
	v_cvt_pk_bf16_f32 v19, v19, v32
	global_store_dword v[16:17], v19, off
.LBB0_900:
	s_or_b64 exec, exec, s[8:9]
	v_mul_f32_e32 v19, v77, v2
	s_waitcnt lgkmcnt(0)
	s_nop 1
	v_mov_b32_dpp v32, v19 quad_perm:[1,0,3,2] row_mask:0xf bank_mask:0xf bound_ctrl:1
	s_and_saveexec_b64 s[8:9], vcc
	s_cbranch_execz .LBB0_902
	s_waitcnt lgkmcnt(0)
	v_cvt_pk_bf16_f32 v19, v19, v32
	global_store_dword v[16:17], v19, off offset:64
; __device__ __forceinline__ unsigned cvtpk(float lo, float hi) { unsigned r; asm volatile("v_cvt_pk_bf16_f32 %0, %1, %2" : "=v"(r) : "v"(lo), "v"(hi)); return r; }
; template <int MODE>
; __device__ __forceinline__ void attn_block_pipe(const BlockRef& cur, const BlockRef& nxt, char* lds, LAS unsigned char* ldsl, Seam<MODE>& S) {
;     ...
; #pragma unroll
;     for (int r = 0; r < 16; ++r) { const size_t ou_ = (size_t)((r & 3) + 8 * (r >> 2)) * cur.os;
; #pragma unroll
;         for (int d0 = 0; d0 < 4; ++d0) { const float v = o[d0][r] * rli[r];
;             const float vn = __shfl_xor(v, 1);
;             if ((r32 & 1) == 0) *(unsigned*)((char*)(Ow + ou_ + d0 * 32) + ol_) = cvtpk(v, vn); } }
.LBB0_902:
	s_or_b64 exec, exec, s[8:9]
	v_mul_f32_e32 v19, v61, v2
	s_waitcnt lgkmcnt(0)
	s_nop 1
	v_mov_b32_dpp v32, v19 quad_perm:[1,0,3,2] row_mask:0xf bank_mask:0xf bound_ctrl:1
	s_and_saveexec_b64 s[8:9], vcc
	s_cbranch_execz .LBB0_904
	s_waitcnt lgkmcnt(0)
	v_cvt_pk_bf16_f32 v19, v19, v32
	global_store_dword v[16:17], v19, off offset:128
.LBB0_904:
	s_or_b64 exec, exec, s[8:9]
	v_mul_f32_e32 v2, v45, v2
	s_nop 1
	v_mov_b32_dpp v19, v2 quad_perm:[1,0,3,2] row_mask:0xf bank_mask:0xf bound_ctrl:1
	s_and_saveexec_b64 s[8:9], vcc
	s_cbranch_execz .LBB0_906
	s_waitcnt lgkmcnt(0)
	v_cvt_pk_bf16_f32 v2, v2, v19
	global_store_dword v[16:17], v2, off offset:192
.LBB0_906:
	s_or_b64 exec, exec, s[8:9]
	v_rcp_f32_e32 v2, v98
	v_lshl_add_u64 v[16:17], v[16:17], 0, s[6:7]
	s_waitcnt lgkmcnt(0)
	v_mul_f32_e32 v19, v94, v2
	s_nop 1
	v_mov_b32_dpp v32, v19 quad_perm:[1,0,3,2] row_mask:0xf bank_mask:0xf bound_ctrl:1
	s_and_saveexec_b64 s[6:7], vcc
	s_cbranch_execz .LBB0_908
	s_waitcnt lgkmcnt(0)
	v_cvt_pk_bf16_f32 v19, v19, v32
	global_store_dword v[16:17], v19, off
.LBB0_908:
	s_or_b64 exec, exec, s[6:7]
	v_mul_f32_e32 v19, v78, v2
	s_waitcnt lgkmcnt(0)
	s_nop 1
	v_mov_b32_dpp v32, v19 quad_perm:[1,0,3,2] row_mask:0xf bank_mask:0xf bound_ctrl:1
	s_and_saveexec_b64 s[6:7], vcc
	s_cbranch_execz .LBB0_910
	s_waitcnt lgkmcnt(0)
	v_cvt_pk_bf16_f32 v19, v19, v32
	global_store_dword v[16:17], v19, off offset:64
.LBB0_910:
	s_or_b64 exec, exec, s[6:7]
	v_mul_f32_e32 v19, v62, v2
	s_waitcnt lgkmcnt(0)
	s_nop 1
	v_mov_b32_dpp v32, v19 quad_perm:[1,0,3,2] row_mask:0xf bank_mask:0xf bound_ctrl:1
	s_and_saveexec_b64 s[6:7], vcc
	s_cbranch_execz .LBB0_912
	s_waitcnt lgkmcnt(0)
	v_cvt_pk_bf16_f32 v19, v19, v32
	global_store_dword v[16:17], v19, off offset:128
.LBB0_912:
	s_or_b64 exec, exec, s[6:7]
	v_mul_f32_e32 v2, v46, v2
	s_nop 1
	v_mov_b32_dpp v19, v2 quad_perm:[1,0,3,2] row_mask:0xf bank_mask:0xf bound_ctrl:1
	s_and_saveexec_b64 s[6:7], vcc
	s_cbranch_execz .LBB0_914
	s_waitcnt lgkmcnt(0)
	v_cvt_pk_bf16_f32 v2, v2, v19
	global_store_dword v[16:17], v2, off offset:192
.LBB0_914:
	s_or_b64 exec, exec, s[6:7]
	v_rcp_f32_e32 v2, v99
	v_lshl_add_u64 v[16:17], v[16:17], 0, s[4:5]
	s_waitcnt lgkmcnt(0)
	v_mul_f32_e32 v19, v95, v2
	s_nop 1
	v_mov_b32_dpp v32, v19 quad_perm:[1,0,3,2] row_mask:0xf bank_mask:0xf bound_ctrl:1
	s_and_saveexec_b64 s[6:7], vcc
	s_cbranch_execz .LBB0_916
	s_waitcnt lgkmcnt(0)
	v_cvt_pk_bf16_f32 v19, v19, v32
	global_store_dword v[16:17], v19, off
.LBB0_916:
	s_or_b64 exec, exec, s[6:7]
	v_mul_f32_e32 v19, v79, v2
	s_waitcnt lgkmcnt(0)
	s_nop 1
	v_mov_b32_dpp v32, v19 quad_perm:[1,0,3,2] row_mask:0xf bank_mask:0xf bound_ctrl:1
	s_and_saveexec_b64 s[6:7], vcc
	s_cbranch_execz .LBB0_918
	s_waitcnt lgkmcnt(0)
	v_cvt_pk_bf16_f32 v19, v19, v32
	global_store_dword v[16:17], v19, off offset:64
.LBB0_918:
	s_or_b64 exec, exec, s[6:7]
	v_mul_f32_e32 v19, v63, v2
	s_waitcnt lgkmcnt(0)
	s_nop 1
	v_mov_b32_dpp v32, v19 quad_perm:[1,0,3,2] row_mask:0xf bank_mask:0xf bound_ctrl:1
	s_and_saveexec_b64 s[6:7], vcc
	s_cbranch_execz .LBB0_920
	s_waitcnt lgkmcnt(0)
	v_cvt_pk_bf16_f32 v19, v19, v32
	global_store_dword v[16:17], v19, off offset:128
.LBB0_920:
	s_or_b64 exec, exec, s[6:7]
	v_mul_f32_e32 v2, v47, v2
	s_nop 1
	v_mov_b32_dpp v19, v2 quad_perm:[1,0,3,2] row_mask:0xf bank_mask:0xf bound_ctrl:1
	s_and_saveexec_b64 s[6:7], vcc
	s_cbranch_execz .LBB0_922
	s_waitcnt lgkmcnt(0)
	v_cvt_pk_bf16_f32 v2, v2, v19
	global_store_dword v[16:17], v2, off offset:192
.LBB0_922:
	s_or_b64 exec, exec, s[6:7]
	v_rcp_f32_e32 v2, v100
	v_lshl_add_u64 v[16:17], v[16:17], 0, s[4:5]
	s_waitcnt lgkmcnt(0)
	v_mul_f32_e32 v19, v96, v2
	s_nop 1
	v_mov_b32_dpp v32, v19 quad_perm:[1,0,3,2] row_mask:0xf bank_mask:0xf bound_ctrl:1
	s_and_saveexec_b64 s[6:7], vcc
	s_cbranch_execz .LBB0_924
	s_waitcnt lgkmcnt(0)
	v_cvt_pk_bf16_f32 v19, v19, v32
	global_store_dword v[16:17], v19, off
.LBB0_924:
	s_or_b64 exec, exec, s[6:7]
	v_mul_f32_e32 v19, v80, v2
	s_waitcnt lgkmcnt(0)
	s_nop 1
	v_mov_b32_dpp v32, v19 quad_perm:[1,0,3,2] row_mask:0xf bank_mask:0xf bound_ctrl:1
	s_and_saveexec_b64 s[6:7], vcc
	s_cbranch_execz .LBB0_926
	s_waitcnt lgkmcnt(0)
	v_cvt_pk_bf16_f32 v19, v19, v32
	global_store_dword v[16:17], v19, off offset:64
.LBB0_926:
	s_or_b64 exec, exec, s[6:7]
	v_mul_f32_e32 v19, v64, v2
	s_waitcnt lgkmcnt(0)
	s_nop 1
	v_mov_b32_dpp v32, v19 quad_perm:[1,0,3,2] row_mask:0xf bank_mask:0xf bound_ctrl:1
	s_and_saveexec_b64 s[6:7], vcc
	s_cbranch_execz .LBB0_928
	s_waitcnt lgkmcnt(0)
	v_cvt_pk_bf16_f32 v19, v19, v32
	global_store_dword v[16:17], v19, off offset:128
.LBB0_928:
	s_or_b64 exec, exec, s[6:7]
	v_mul_f32_e32 v2, v48, v2
	s_nop 1
	v_mov_b32_dpp v19, v2 quad_perm:[1,0,3,2] row_mask:0xf bank_mask:0xf bound_ctrl:1
	s_and_saveexec_b64 s[6:7], vcc
	s_cbranch_execz .LBB0_930
	s_waitcnt lgkmcnt(0)
	v_cvt_pk_bf16_f32 v2, v2, v19
	global_store_dword v[16:17], v2, off offset:192
.LBB0_930:
	s_or_b64 exec, exec, s[6:7]
	v_rcp_f32_e32 v2, v101
	v_lshl_add_u64 v[16:17], v[16:17], 0, s[4:5]
	s_waitcnt lgkmcnt(0)
	v_mul_f32_e32 v19, v97, v2
	s_nop 1
	v_mov_b32_dpp v32, v19 quad_perm:[1,0,3,2] row_mask:0xf bank_mask:0xf bound_ctrl:1
	s_and_saveexec_b64 s[4:5], vcc
	s_cbranch_execz .LBB0_932
	s_waitcnt lgkmcnt(0)
	v_cvt_pk_bf16_f32 v19, v19, v32
	global_store_dword v[16:17], v19, off
.LBB0_932:
	s_or_b64 exec, exec, s[4:5]
	v_mul_f32_e32 v19, v81, v2
	s_waitcnt lgkmcnt(0)
	s_nop 1
	v_mov_b32_dpp v32, v19 quad_perm:[1,0,3,2] row_mask:0xf bank_mask:0xf bound_ctrl:1
	s_and_saveexec_b64 s[4:5], vcc
	s_cbranch_execz .LBB0_934
	s_waitcnt lgkmcnt(0)
	v_cvt_pk_bf16_f32 v19, v19, v32
	global_store_dword v[16:17], v19, off offset:64
.LBB0_934:
	s_or_b64 exec, exec, s[4:5]
	v_mul_f32_e32 v19, v65, v2
	s_waitcnt lgkmcnt(0)
	s_nop 1
	v_mov_b32_dpp v32, v19 quad_perm:[1,0,3,2] row_mask:0xf bank_mask:0xf bound_ctrl:1
	s_and_saveexec_b64 s[4:5], vcc
	s_cbranch_execz .LBB0_936
	s_waitcnt lgkmcnt(0)
	v_cvt_pk_bf16_f32 v19, v19, v32
	global_store_dword v[16:17], v19, off offset:128
.LBB0_936:
	s_or_b64 exec, exec, s[4:5]
	v_mul_f32_e32 v2, v49, v2
	s_nop 1
	v_mov_b32_dpp v1, v2 quad_perm:[1,0,3,2] row_mask:0xf bank_mask:0xf bound_ctrl:1
	s_and_saveexec_b64 s[4:5], vcc
	s_cbranch_execz .LBB0_714
	s_waitcnt lgkmcnt(0)
	v_cvt_pk_bf16_f32 v1, v2, v1
	global_store_dword v[16:17], v1, off offset:192
	s_branch .LBB0_714

; __device__ __forceinline__ int crow(int r, int hi) { return (r & 3) + 8 * (r >> 2) + 4 * hi; }
; __device__ __forceinline__ unsigned cvtpk(float lo, float hi) { unsigned r; asm volatile("v_cvt_pk_bf16_f32 %0, %1, %2" : "=v"(r) : "v"(lo), "v"(hi)); return r; }
; template <int MODE>
; __device__ __forceinline__ void attn_block_pipe(const BlockRef& cur, const BlockRef& nxt, char* lds, LAS unsigned char* ldsl, Seam<MODE>& S) {
;     ...
;     if (hi == 0) li_l[r32] = l_reg; asm volatile("s_waitcnt lgkmcnt(0)" ::: "memory");
;     if constexpr (C::ALIBI) { if (hi == 0) cur.LSE[(size_t)(qlo + r32) * cur.ls] = m_reg * SCALE + __logf(l_reg); }
;     float rli[16];
; #pragma unroll
;     for (int r = 0; r < 16; ++r) rli[r] = __builtin_amdgcn_rcpf(li_l[crow(r, hi)]);
;     bf16_t* Ow = cur.O + (size_t)qlo * cur.os;
;     const unsigned ol_ = (unsigned)(4 * hi * cur.os + r32) * 2u;
; #pragma unroll
;     for (int r = 0; r < 16; ++r) { const size_t ou_ = (size_t)((r & 3) + 8 * (r >> 2)) * cur.os;
; #pragma unroll
;         for (int d0 = 0; d0 < 4; ++d0) { const float v = o[d0][r] * rli[r];
;             const float vn = __shfl_xor(v, 1);
;             if ((r32 & 1) == 0) *(unsigned*)((char*)(Ow + ou_ + d0 * 32) + ol_) = cvtpk(v, vn); } }
.LBB0_1062:
	s_waitcnt vmcnt(12)
	v_cmp_gt_u32_e32 vcc, 32, v206
	s_and_saveexec_b64 s[4:5], vcc
	ds_write_b32 v208, v2
	s_or_b64 exec, exec, s[4:5]
	s_waitcnt lgkmcnt(0)
	ds_read_b128 v[94:97], v207
	v_and_b32_e32 v17, 64, v1
	v_xor_b32_e32 v16, 1, v1
	v_add_u32_e32 v17, 64, v17
	v_cmp_lt_i32_e32 vcc, v16, v17
	s_waitcnt lgkmcnt(0)
	v_rcp_f32_e32 v98, v94
	ds_read_b128 v[90:93], v207 offset:32
	ds_read_b128 v[86:89], v207 offset:64
	ds_read_b128 v[82:85], v207 offset:96
	v_cndmask_b32_e32 v16, v1, v16, vcc
	v_lshlrev_b32_e32 v94, 2, v16
	v_mul_f32_e32 v66, v66, v98
	s_ashr_i32 s41, s40, 31
	s_nop 1
	v_mov_b32_dpp v99, v66 quad_perm:[1,0,3,2] row_mask:0xf bank_mask:0xf bound_ctrl:1
	s_lshl_b64 s[4:5], s[40:41], 11
	s_add_u32 s6, s38, s4
	v_lshlrev_b32_e32 v2, 1, v205
	s_addc_u32 s7, s39, s5
	v_lshl_or_b32 v2, v204, 13, v2
	v_and_b32_e32 v16, 1, v203
	v_cmp_eq_u32_e64 s[4:5], 0, v16
	v_lshl_add_u64 v[16:17], s[6:7], 0, v[2:3]
	s_and_saveexec_b64 s[6:7], s[4:5]
	s_cbranch_execz .LBB0_1066
	s_waitcnt lgkmcnt(0)
	v_cvt_pk_bf16_f32 v2, v66, v99
	global_store_dword v[16:17], v2, off
